# speedup vs baseline: 1.0470x; 1.0206x over previous
.LBB0_95:
	s_andn2_b64 vcc, exec, s[4:5]
	s_cbranch_vccnz .LBB0_106
	v_lshl_or_b32 v2, s2, 8, v0
	v_ashrrev_i32_e32 v3, 31, v2
	v_and_b32_e32 v27, 0xe0, v0
	s_waitcnt lgkmcnt(0)
	s_lshl_b32 s30, s2, 2
	s_add_u32 s28, s28, s30
	s_addc_u32 s29, s29, 0
	s_load_dword s30, s[28:29], 0x0
	v_lshl_add_u64 v[2:3], v[2:3], 2, s[20:21]
	v_and_b32_e32 v1, 31, v0
	v_mov_b32_e32 v107, 0
	v_lshlrev_b32_e32 v106, 9, v27
	global_load_dword v26, v[2:3], off
	v_lshl_add_u64 v[2:3], s[22:23], 0, v[106:107]
	v_lshlrev_b32_e32 v106, 4, v1
	s_movk_i32 s3, 0x1000
	v_lshl_add_u64 v[22:23], v[2:3], 0, v[106:107]
	v_add_co_u32_e32 v24, vcc, s3, v22
	global_load_dwordx4 v[38:41], v[22:23], off
	global_load_dwordx4 v[98:101], v[22:23], off offset:512
	global_load_dwordx4 v[54:57], v[22:23], off offset:2048
	global_load_dwordx4 v[90:93], v[22:23], off offset:2560
	v_addc_co_u32_e32 v25, vcc, 0, v23, vcc
	global_load_dwordx4 v[70:73], v[24:25], off offset:512
	s_movk_i32 s4, 0x2000
	v_add_co_u32_e32 v108, vcc, s4, v22
	v_lshlrev_b32_e32 v112, 2, v0
	s_nop 0
	v_addc_co_u32_e32 v109, vcc, 0, v23, vcc
	global_load_dwordx4 v[82:85], v[108:109], off offset:-4096
	global_load_dwordx4 v[78:81], v[22:23], off offset:1024
	global_load_dwordx4 v[74:77], v[22:23], off offset:3072
	global_load_dwordx4 v[86:89], v[24:25], off offset:1024
	global_load_dwordx4 v[18:21], v[24:25], off offset:2560
	global_load_dwordx4 v[14:17], v[24:25], off offset:2048
	global_load_dwordx4 v[10:13], v[24:25], off offset:3072
	global_load_dwordx4 v[6:9], v[22:23], off offset:1536
	global_load_dwordx4 v[2:5], v[24:25], off offset:1536
	v_lshlrev_b32_e32 v113, 2, v27
	global_load_dwordx4 v[62:65], v[22:23], off offset:3584
	global_load_dwordx4 v[42:45], v[24:25], off offset:3584
	s_movk_i32 s3, 0x3000
	v_add_co_u32_e32 v122, vcc, s3, v22
	s_load_dwordx2 s[4:5], s[0:1], 0x18
	s_nop 0
	v_addc_co_u32_e32 v123, vcc, 0, v23, vcc
	s_movk_i32 s0, 0x7f
	s_movk_i32 s1, 0x80
	v_cmp_lt_u32_e32 vcc, s0, v0
	v_cmp_gt_u32_e64 s[0:1], s1, v0
	s_waitcnt vmcnt(16)
	ds_write_b32 v112, v26 offset:32768
	s_waitcnt lgkmcnt(0)
	s_barrier
	ds_read_b128 v[114:117], v113 offset:32768
	ds_read_b128 v[118:121], v113 offset:32784
	ds_read_b128 v[102:105], v113 offset:32800
	ds_read_b128 v[94:97], v113 offset:32816
	global_load_dwordx4 v[22:25], v[108:109], off
	global_load_dwordx4 v[46:49], v[108:109], off offset:512
	global_load_dwordx4 v[26:29], v[108:109], off offset:2048
	global_load_dwordx4 v[50:53], v[108:109], off offset:2560
	global_load_dwordx4 v[30:33], v[122:123], off
	global_load_dwordx4 v[58:61], v[122:123], off offset:512
	global_load_dwordx4 v[34:37], v[122:123], off offset:2048
	global_load_dwordx4 v[66:69], v[122:123], off offset:2560
	s_waitcnt vmcnt(22) lgkmcnt(3)
	v_pk_mul_f32 v[100:101], v[114:115], v[100:101] op_sel:[1,0]
	v_pk_mul_f32 v[98:99], v[114:115], v[98:99] op_sel:[1,0]
	v_pk_fma_f32 v[100:101], v[114:115], v[40:41], v[100:101] op_sel_hi:[0,1,1]
	v_pk_fma_f32 v[98:99], v[114:115], v[38:39], v[98:99] op_sel_hi:[0,1,1]
	global_load_dwordx4 v[38:41], v[108:109], off offset:1024
	s_waitcnt vmcnt(21) lgkmcnt(2)
	v_pk_mul_f32 v[92:93], v[118:119], v[92:93] op_sel:[1,0]
	v_pk_mul_f32 v[90:91], v[118:119], v[90:91] op_sel:[1,0]
	s_waitcnt vmcnt(20) lgkmcnt(1)
	v_pk_mul_f32 v[72:73], v[102:103], v[72:73] op_sel:[1,0]
	v_pk_mul_f32 v[70:71], v[102:103], v[70:71] op_sel:[1,0]
	v_pk_fma_f32 v[92:93], v[118:119], v[56:57], v[92:93] op_sel_hi:[0,1,1]
	v_pk_fma_f32 v[90:91], v[118:119], v[54:55], v[90:91] op_sel_hi:[0,1,1]
	global_load_dwordx4 v[54:57], v[108:109], off offset:3072
	s_waitcnt vmcnt(20)
	v_pk_fma_f32 v[114:115], v[102:103], v[84:85], v[72:73] op_sel_hi:[0,1,1]
	v_pk_fma_f32 v[118:119], v[102:103], v[82:83], v[70:71] op_sel_hi:[0,1,1]
	global_load_dwordx4 v[70:73], v[122:123], off offset:1024
	s_waitcnt vmcnt(20)
	v_pk_fma_f32 v[124:125], v[116:117], v[80:81], v[100:101] op_sel_hi:[0,1,1]
	v_pk_fma_f32 v[126:127], v[116:117], v[78:79], v[98:99] op_sel_hi:[0,1,1]
	global_load_dwordx4 v[78:81], v[122:123], off offset:3072
	s_waitcnt vmcnt(20)
	v_pk_fma_f32 v[102:103], v[120:121], v[76:77], v[92:93] op_sel_hi:[0,1,1]
	v_pk_fma_f32 v[110:111], v[120:121], v[74:75], v[90:91] op_sel_hi:[0,1,1]
	global_load_dwordx4 v[82:85], v[108:109], off offset:1536
	global_load_dwordx4 v[74:77], v[108:109], off offset:3584
	s_waitcnt vmcnt(21)
	v_pk_fma_f32 v[98:99], v[104:105], v[88:89], v[114:115] op_sel_hi:[0,1,1]
	v_pk_fma_f32 v[100:101], v[104:105], v[86:87], v[118:119] op_sel_hi:[0,1,1]
	global_load_dwordx4 v[86:89], v[122:123], off offset:1536
	global_load_dwordx4 v[90:93], v[122:123], off offset:3584
	s_waitcnt vmcnt(22) lgkmcnt(0)
	v_pk_mul_f32 v[20:21], v[94:95], v[20:21] op_sel:[1,0]
	v_pk_mul_f32 v[18:19], v[94:95], v[18:19] op_sel:[1,0]
	v_mov_b32_e32 v114, v117
	s_waitcnt vmcnt(21)
	v_pk_fma_f32 v[16:17], v[94:95], v[16:17], v[20:21] op_sel_hi:[0,1,1]
	v_pk_fma_f32 v[14:15], v[94:95], v[14:15], v[18:19] op_sel_hi:[0,1,1]
	v_mov_b32_e32 v116, v121
	s_waitcnt vmcnt(20)
	v_pk_fma_f32 v[94:95], v[96:97], v[12:13], v[16:17] op_sel_hi:[0,1,1]
	v_pk_fma_f32 v[120:121], v[96:97], v[10:11], v[14:15] op_sel_hi:[0,1,1]
	ds_read_b128 v[10:13], v113 offset:32832
	ds_read_b128 v[14:17], v113 offset:32848
	s_waitcnt vmcnt(19)
	v_pk_fma_f32 v[122:123], v[114:115], v[8:9], v[124:125] op_sel_hi:[0,1,1]
	v_pk_fma_f32 v[114:115], v[114:115], v[6:7], v[126:127] op_sel_hi:[0,1,1]
	ds_read_b128 v[6:9], v113 offset:32864
	ds_read_b128 v[18:21], v113 offset:32880
	v_mov_b32_e32 v96, v97
	v_mov_b32_e32 v118, v105
	s_waitcnt vmcnt(17)
	v_pk_fma_f32 v[64:65], v[116:117], v[64:65], v[102:103] op_sel_hi:[0,1,1]
	v_pk_fma_f32 v[62:63], v[116:117], v[62:63], v[110:111] op_sel_hi:[0,1,1]
	s_waitcnt vmcnt(16)
	v_pk_fma_f32 v[44:45], v[96:97], v[44:45], v[94:95] op_sel_hi:[0,1,1]
	v_pk_fma_f32 v[42:43], v[96:97], v[42:43], v[120:121] op_sel_hi:[0,1,1]
	v_pk_add_f32 v[94:95], v[122:123], 0 op_sel_hi:[1,0]
	v_pk_add_f32 v[96:97], v[114:115], 0 op_sel_hi:[1,0]
	v_pk_fma_f32 v[4:5], v[118:119], v[4:5], v[98:99] op_sel_hi:[0,1,1]
	v_pk_fma_f32 v[2:3], v[118:119], v[2:3], v[100:101] op_sel_hi:[0,1,1]
	v_pk_add_f32 v[64:65], v[94:95], v[64:65]
	v_pk_add_f32 v[62:63], v[96:97], v[62:63]
	v_pk_add_f32 v[4:5], v[64:65], v[4:5]
	v_pk_add_f32 v[2:3], v[62:63], v[2:3]
	v_pk_add_f32 v[4:5], v[4:5], v[44:45]
	v_pk_add_f32 v[2:3], v[2:3], v[42:43]
	v_lshrrev_b32_e32 v104, 5, v0
	v_lshl_or_b32 v105, v104, 9, v106
	s_waitcnt lgkmcnt(3)
	v_mov_b32_e32 v106, v13
	s_waitcnt lgkmcnt(2)
	v_mov_b32_e32 v102, v17
	s_waitcnt lgkmcnt(1)
	v_mov_b32_e32 v110, v9
	s_waitcnt lgkmcnt(0)
	v_mov_b32_e32 v116, v21
	v_or_b32_e32 v108, 0x8000, v112
	s_waitcnt vmcnt(14)
	v_pk_mul_f32 v[42:43], v[10:11], v[48:49] op_sel:[1,0]
	v_pk_mul_f32 v[44:45], v[10:11], v[46:47] op_sel:[1,0]
	s_waitcnt vmcnt(12)
	v_pk_mul_f32 v[46:47], v[14:15], v[52:53] op_sel:[1,0]
	v_pk_mul_f32 v[48:49], v[14:15], v[50:51] op_sel:[1,0]
	s_waitcnt vmcnt(10)
	v_pk_mul_f32 v[50:51], v[6:7], v[60:61] op_sel:[1,0]
	v_pk_mul_f32 v[52:53], v[6:7], v[58:59] op_sel:[1,0]
	s_waitcnt vmcnt(8)
	v_pk_mul_f32 v[58:59], v[18:19], v[68:69] op_sel:[1,0]
	v_pk_mul_f32 v[60:61], v[18:19], v[66:67] op_sel:[1,0]
	v_pk_fma_f32 v[24:25], v[10:11], v[24:25], v[42:43] op_sel_hi:[0,1,1]
	v_pk_fma_f32 v[10:11], v[10:11], v[22:23], v[44:45] op_sel_hi:[0,1,1]
	v_pk_fma_f32 v[22:23], v[14:15], v[28:29], v[46:47] op_sel_hi:[0,1,1]
	v_pk_fma_f32 v[14:15], v[14:15], v[26:27], v[48:49] op_sel_hi:[0,1,1]
	v_pk_fma_f32 v[26:27], v[6:7], v[32:33], v[50:51] op_sel_hi:[0,1,1]
	v_pk_fma_f32 v[6:7], v[6:7], v[30:31], v[52:53] op_sel_hi:[0,1,1]
	v_pk_fma_f32 v[28:29], v[18:19], v[36:37], v[58:59] op_sel_hi:[0,1,1]
	v_pk_fma_f32 v[18:19], v[18:19], v[34:35], v[60:61] op_sel_hi:[0,1,1]
	s_waitcnt vmcnt(7)
	v_pk_fma_f32 v[24:25], v[12:13], v[40:41], v[24:25] op_sel_hi:[0,1,1]
	v_pk_fma_f32 v[10:11], v[12:13], v[38:39], v[10:11] op_sel_hi:[0,1,1]
	s_waitcnt vmcnt(6)
	v_pk_fma_f32 v[12:13], v[16:17], v[56:57], v[22:23] op_sel_hi:[0,1,1]
	v_pk_fma_f32 v[14:15], v[16:17], v[54:55], v[14:15] op_sel_hi:[0,1,1]
	s_waitcnt vmcnt(5)
	v_pk_fma_f32 v[16:17], v[8:9], v[72:73], v[26:27] op_sel_hi:[0,1,1]
	v_pk_fma_f32 v[6:7], v[8:9], v[70:71], v[6:7] op_sel_hi:[0,1,1]
	s_waitcnt vmcnt(4)
	v_pk_fma_f32 v[8:9], v[20:21], v[80:81], v[28:29] op_sel_hi:[0,1,1]
	v_pk_fma_f32 v[18:19], v[20:21], v[78:79], v[18:19] op_sel_hi:[0,1,1]
	s_waitcnt vmcnt(3)
	v_pk_fma_f32 v[20:21], v[106:107], v[84:85], v[24:25] op_sel_hi:[0,1,1]
	v_pk_fma_f32 v[10:11], v[106:107], v[82:83], v[10:11] op_sel_hi:[0,1,1]
	s_waitcnt vmcnt(2)
	v_pk_fma_f32 v[12:13], v[102:103], v[76:77], v[12:13] op_sel_hi:[0,1,1]
	v_pk_fma_f32 v[14:15], v[102:103], v[74:75], v[14:15] op_sel_hi:[0,1,1]
	v_pk_add_f32 v[4:5], v[4:5], v[20:21]
	v_pk_add_f32 v[2:3], v[2:3], v[10:11]
	s_waitcnt vmcnt(1)
	v_pk_fma_f32 v[16:17], v[110:111], v[88:89], v[16:17] op_sel_hi:[0,1,1]
	v_pk_fma_f32 v[6:7], v[110:111], v[86:87], v[6:7] op_sel_hi:[0,1,1]
	v_pk_add_f32 v[4:5], v[4:5], v[12:13]
	v_pk_add_f32 v[2:3], v[2:3], v[14:15]
	s_waitcnt vmcnt(0)
	v_pk_fma_f32 v[8:9], v[116:117], v[92:93], v[8:9] op_sel_hi:[0,1,1]
	v_pk_fma_f32 v[18:19], v[116:117], v[90:91], v[18:19] op_sel_hi:[0,1,1]
	v_pk_add_f32 v[4:5], v[4:5], v[16:17]
	v_pk_add_f32 v[2:3], v[2:3], v[6:7]
	v_pk_add_f32 v[4:5], v[4:5], v[8:9]
	v_pk_add_f32 v[2:3], v[2:3], v[18:19]
	ds_write_b128 v105, v[2:5]
	s_waitcnt lgkmcnt(0)
	s_barrier
	s_and_saveexec_b64 s[6:7], s[0:1]
	s_cbranch_execz .LBB0_98
	ds_read2st64_b32 v[2:3], v112 offset1:2
	ds_read2st64_b32 v[4:5], v112 offset0:4 offset1:6
	ds_read2st64_b32 v[6:7], v112 offset0:8 offset1:10
	ds_read2st64_b32 v[8:9], v112 offset0:12 offset1:14
	s_waitcnt lgkmcnt(3)
	v_add_f32_e32 v2, v2, v3
	s_waitcnt lgkmcnt(2)
	v_add_f32_e32 v3, v4, v5
	v_add_f32_e32 v2, v2, v3
	s_waitcnt lgkmcnt(1)
	v_add_f32_e32 v3, v6, v7
	s_waitcnt lgkmcnt(0)
	v_add_f32_e32 v4, v8, v9
	v_add_f32_e32 v3, v3, v4
	v_add_f32_e32 v2, v2, v3
	ds_write2st64_b32 v108, v2, v107 offset0:8 offset1:10
.LBB0_98:
	s_or_b64 exec, exec, s[6:7]
	s_ashr_i32 s3, s2, 31
	s_lshl_b64 s[0:1], s[2:3], 2
	s_add_u32 s0, s4, s0
	s_addc_u32 s1, s5, s1
	s_waitcnt lgkmcnt(0)
	s_barrier
	s_ashr_i32 s0, s2, 6
	s_bfe_u32 s1, s2, 0x20004
	s_mul_i32 s0, s0, 20
	s_mul_i32 s9, s1, 5
	s_bfe_u32 s8, s2, 0x10003
	s_and_b32 s6, s2, 7
	s_add_i32 s9, s9, s0
	s_mov_b64 s[2:3], 0
	s_and_saveexec_b64 s[0:1], vcc
	s_xor_b64 s[0:1], exec, s[0:1]
	s_cbranch_execz .LBB0_107
	s_movk_i32 s2, 0xa0
	v_cmp_gt_u32_e32 vcc, s2, v0
	s_mov_b64 s[4:5], 0
	s_and_saveexec_b64 s[2:3], vcc
	s_cbranch_execz .LBB0_103
	s_movk_i32 s4, 0x88
	v_add_u32_e32 v1, 0xffffff80, v0
	v_cmp_gt_u32_e32 vcc, s4, v0
	v_mov_b32_e32 v0, 0
	s_and_saveexec_b64 s[4:5], vcc
	s_cbranch_execz .LBB0_102
	v_lshlrev_b32_e32 v0, 7, v1
	ds_read_b128 v[2:5], v0 offset:32768
	ds_read_b128 v[6:9], v0 offset:32784
	ds_read_b128 v[10:13], v0 offset:32800
	ds_read_b128 v[14:17], v0 offset:32816
	ds_read_b128 v[18:21], v0 offset:32832
	s_waitcnt lgkmcnt(0)
	v_add_f32_e32 v2, 0, v2
	v_add_f32_e32 v2, v2, v3
	v_add_f32_e32 v2, v2, v4
	v_add_f32_e32 v2, v2, v5
	v_add_f32_e32 v2, v2, v6
	v_add_f32_e32 v2, v2, v7
	v_add_f32_e32 v2, v2, v8
	v_add_f32_e32 v2, v2, v9
	v_add_f32_e32 v2, v2, v10
	v_add_f32_e32 v2, v2, v11
	v_add_f32_e32 v2, v2, v12
	v_add_f32_e32 v2, v2, v13
	v_add_f32_e32 v2, v2, v14
	v_add_f32_e32 v2, v2, v15
	v_add_f32_e32 v2, v2, v16
	v_add_f32_e32 v6, v2, v17
	ds_read_b128 v[2:5], v0 offset:32848
	v_add_f32_e32 v6, v6, v18
	v_add_f32_e32 v6, v6, v19
	v_add_f32_e32 v6, v6, v20
	v_add_f32_e32 v6, v6, v21
	s_waitcnt lgkmcnt(0)
	v_add_f32_e32 v2, v6, v2
	ds_read_b128 v[6:9], v0 offset:32864
	v_add_f32_e32 v2, v2, v3
	v_add_f32_e32 v2, v2, v4
	v_add_f32_e32 v10, v2, v5
	ds_read_b128 v[2:5], v0 offset:32880
	s_waitcnt lgkmcnt(1)
	v_add_f32_e32 v0, v10, v6
	v_add_f32_e32 v0, v0, v7
	v_add_f32_e32 v0, v0, v8
	v_add_f32_e32 v0, v0, v9
	s_waitcnt lgkmcnt(0)
	v_add_f32_e32 v0, v0, v2
	v_add_f32_e32 v0, v0, v3
	v_add_f32_e32 v0, v0, v4
	v_add_f32_e32 v0, v0, v5
	v_mul_f32_e32 v0, s30, v0

.LBB0_108:
	ds_read2st64_b32 v[2:3], v108 offset0:8 offset1:10
	v_lshlrev_b32_e32 v1, 3, v1
	s_movk_i32 s4, 0x7fff
	v_add_lshl_u32 v0, s9, v104, 9
	v_lshl_or_b32 v1, s8, 8, v1
	s_waitcnt lgkmcnt(0)
	v_add_f32_e32 v2, v2, v3
	v_mul_f32_e32 v2, s30, v2
	v_bfe_u32 v3, v2, 16, 1
	v_add3_u32 v4, v2, v3, s4
	v_or3_b32 v2, v0, v1, s6
	s_or_b64 s[2:3], s[2:3], exec
	s_or_b64 exec, exec, s[0:1]
	s_and_saveexec_b64 s[0:1], s[2:3]
	s_cbranch_execnz .LBB0_105
	s_branch .LBB0_106
.Lpre_roleA_pre:
	s_load_dwordx2 s[28:29], s[0:1], 0x18
	s_branch .Lpre_orig

.Ledge_nosum:
	s_waitcnt lgkmcnt(0)
	s_barrier
	ds_read_b128 v[6:9], v176
	ds_read_b128 v[10:13], v176 offset:1024
	ds_read_b128 v[14:17], v176 offset:2048
	ds_read_b128 v[194:197], v176 offset:3072
	ds_read_b128 v[198:201], v189 offset:57344
	ds_read_b128 v[18:21], v189 offset:57360
	ds_read_b128 v[202:205], v176 offset:4096
	ds_read_b128 v[206:209], v176 offset:5120
	ds_read_b128 v[210:213], v176 offset:6144
	ds_read_b128 v[214:217], v176 offset:7168
	ds_read_b128 v[218:221], v189 offset:57408
	ds_read_b128 v[222:225], v189 offset:57424
	s_movk_i32 s0, 0x1200
	v_and_b32_e32 v188, 31, v0
	v_lshlrev_b32_e32 v226, 16, v2
	v_and_b32_e32 v227, 0xffff0000, v2
	v_lshlrev_b32_e32 v22, 16, v3
	v_and_b32_e32 v23, 0xffff0000, v3
	v_lshlrev_b32_e32 v2, 16, v4
	v_and_b32_e32 v3, 0xffff0000, v4
	v_lshlrev_b32_e32 v4, 16, v5
	v_and_b32_e32 v5, 0xffff0000, v5
	s_waitcnt lgkmcnt(0)
	v_pk_mul_f32 v[228:229], v[18:19], v[2:3]
	v_pk_mul_f32 v[18:19], v[20:21], v[4:5]
	v_pk_mul_f32 v[24:25], v[200:201], v[22:23]
	v_pk_mul_f32 v[26:27], v[198:199], v[226:227]
	v_cvt_pk_bf16_f32 v4, v228, v229
	v_pk_fma_f32 v[246:247], v[200:201], v[22:23], v[18:19]
	v_pk_fma_f32 v[248:249], v[198:199], v[226:227], v[228:229]
	ds_read_b128 v[198:201], v176 offset:8192
	ds_read_b128 v[226:229], v176 offset:9216
	ds_read_b128 v[230:233], v176 offset:10240
	ds_read_b128 v[234:237], v176 offset:11264
	ds_read_b128 v[238:241], v189 offset:57472
	ds_read_b128 v[242:245], v189 offset:57488
	v_cvt_pk_bf16_f32 v2, v26, v27
	v_cvt_pk_bf16_f32 v5, v18, v19
	v_cvt_pk_bf16_f32 v3, v24, v25
	s_nop 1
	v_mfma_f32_32x32x16_bf16 v[50:65], v[6:9], v[2:5], 0
	v_mfma_f32_32x32x16_bf16 v[34:49], v[10:13], v[2:5], 0
	v_mfma_f32_32x32x16_bf16 v[18:33], v[14:17], v[2:5], 0
	v_mfma_f32_32x32x16_bf16 v[2:17], v[194:197], v[2:5], 0
	v_lshlrev_b32_e32 v194, 16, v172
	v_and_b32_e32 v195, 0xffff0000, v172
	v_lshlrev_b32_e32 v172, 16, v173
	v_and_b32_e32 v173, 0xffff0000, v173
	v_lshlrev_b32_e32 v250, 16, v170
	v_and_b32_e32 v251, 0xffff0000, v170
	v_lshlrev_b32_e32 v170, 16, v171
	v_and_b32_e32 v171, 0xffff0000, v171
	v_pk_mul_f32 v[222:223], v[222:223], v[194:195]
	v_pk_mul_f32 v[172:173], v[224:225], v[172:173]
	v_pk_mul_f32 v[252:253], v[220:221], v[170:171]
	v_pk_mul_f32 v[254:255], v[218:219], v[250:251]
	v_cvt_pk_bf16_f32 v197, v172, v173
	v_pk_fma_f32 v[170:171], v[220:221], v[170:171], v[172:173]
	v_pk_fma_f32 v[172:173], v[218:219], v[250:251], v[222:223]
	v_cvt_pk_bf16_f32 v196, v222, v223
	v_cvt_pk_bf16_f32 v194, v254, v255
	v_cvt_pk_bf16_f32 v195, v252, v253
	v_pk_add_f32 v[172:173], v[248:249], v[172:173]
	v_pk_add_f32 v[170:171], v[246:247], v[170:171]
	v_mfma_f32_32x32x16_bf16 v[50:65], v[202:205], v[194:197], v[50:65]
	v_pk_mov_b32 v[202:203], v[172:173], v[170:171] op_sel:[1,0]
	v_mov_b32_e32 v173, v171
	v_pk_add_f32 v[170:171], v[202:203], v[172:173]
	s_nop 0
	v_pk_add_f32 v[170:171], v[170:171], v[170:171] op_sel:[0,1] op_sel_hi:[1,0]
	v_mfma_f32_32x32x16_bf16 v[34:49], v[206:209], v[194:197], v[34:49]
	v_mfma_f32_32x32x16_bf16 v[18:33], v[210:213], v[194:197], v[18:33]
	ds_read_b128 v[202:205], v176 offset:12288
	ds_read_b128 v[206:209], v176 offset:13312
	ds_read_b128 v[210:213], v176 offset:14336
	ds_read_b128 v[218:221], v176 offset:15360
	ds_read_b128 v[222:225], v189 offset:57536
	ds_read_b128 v[246:249], v189 offset:57552
	v_mfma_f32_32x32x16_bf16 v[2:17], v[214:217], v[194:197], v[2:17]
	v_lshlrev_b32_e32 v172, 16, v166
	v_and_b32_e32 v173, 0xffff0000, v166
	v_lshlrev_b32_e32 v194, 16, v167
	v_and_b32_e32 v195, 0xffff0000, v167
	v_lshlrev_b32_e32 v166, 16, v168
	v_and_b32_e32 v167, 0xffff0000, v168
	v_lshlrev_b32_e32 v168, 16, v169
	v_and_b32_e32 v169, 0xffff0000, v169
	s_waitcnt lgkmcnt(0)
	v_pk_mul_f32 v[196:197], v[240:241], v[194:195]
	v_pk_mul_f32 v[214:215], v[238:239], v[172:173]
	v_pk_mul_f32 v[216:217], v[242:243], v[166:167]
	v_pk_mul_f32 v[242:243], v[244:245], v[168:169]
	v_cvt_pk_bf16_f32 v168, v216, v217
	v_cvt_pk_bf16_f32 v166, v214, v215
	v_cvt_pk_bf16_f32 v169, v242, v243
	v_cvt_pk_bf16_f32 v167, v196, v197
	v_pk_fma_f32 v[194:195], v[240:241], v[194:195], v[242:243]
	v_pk_fma_f32 v[172:173], v[238:239], v[172:173], v[216:217]
	v_mfma_f32_32x32x16_bf16 v[50:65], v[198:201], v[166:169], v[50:65]
	v_mfma_f32_32x32x16_bf16 v[34:49], v[226:229], v[166:169], v[34:49]
	v_mfma_f32_32x32x16_bf16 v[18:33], v[230:233], v[166:169], v[18:33]
	v_mfma_f32_32x32x16_bf16 v[2:17], v[234:237], v[166:169], v[2:17]
	v_lshlrev_b32_e32 v166, 16, v164
	v_and_b32_e32 v167, 0xffff0000, v164
	v_lshlrev_b32_e32 v164, 16, v165
	v_and_b32_e32 v165, 0xffff0000, v165
	v_mul_f32_e64 v216, v248, v164
	v_mul_f32_e64 v217, v249, v165
	v_mul_u32_u24_e32 v164, 0x140, v192
	v_lshlrev_b32_e32 v164, 4, v164
	v_mov_b32_e32 v165, v175
	v_mul_u32_u24_e32 v171, 0x1400, v192
	v_lshl_add_u64 v[164:165], s[10:11], 0, v[164:165]
	v_readfirstlane_b32 s2, v171
	v_lshlrev_b32_e32 v196, 16, v162
	v_and_b32_e32 v197, 0xffff0000, v162
	v_lshlrev_b32_e32 v162, 16, v163
	v_and_b32_e32 v163, 0xffff0000, v163
	v_lshl_add_u64 v[164:165], v[164:165], 0, v[176:177]
	s_movk_i32 s1, 0x1400
	s_mov_b32 m0, s2
	v_mov_b32_e32 v171, 0x1000
	v_pk_mul_f32 v[198:199], v[224:225], v[162:163]
	s_waitcnt lgkmcnt(0)
	s_barrier
	global_load_lds_dwordx4 v[164:165], off
	global_load_lds_dwordx4 v[164:165], off offset:1024
	global_load_lds_dwordx4 v[164:165], off offset:2048
	global_load_lds_dwordx4 v[164:165], off offset:3072
	s_mov_b64 s[2:3], 0x1000
	v_mad_u32_u24 v171, v192, s1, v171
	v_pk_mul_f32 v[214:215], v[246:247], v[166:167]
	v_cvt_pk_bf16_f32 v167, v198, v199
	v_lshl_add_u64 v[198:199], v[164:165], 0, s[2:3]
	v_readfirstlane_b32 s2, v171
	s_mov_b32 m0, s2
	v_pk_mul_f32 v[200:201], v[222:223], v[196:197]
	global_load_lds_dwordx4 v[198:199], off
	v_pk_fma_f32 v[162:163], v[224:225], v[162:163], v[216:217]
	v_pk_fma_f32 v[196:197], v[222:223], v[196:197], v[214:215]
	v_pk_add_f32 v[162:163], v[194:195], v[162:163]
	v_pk_add_f32 v[172:173], v[172:173], v[196:197]
	v_cvt_pk_bf16_f32 v168, v214, v215
	v_cvt_pk_bf16_f32 v166, v200, v201
	v_cvt_pk_bf16_f32 v169, v216, v217
	v_pk_mov_b32 v[194:195], v[172:173], v[162:163] op_sel:[1,0]
	v_mov_b32_e32 v173, v163
	v_mfma_f32_32x32x16_bf16 v[50:65], v[202:205], v[166:169], v[50:65]
	v_add_f32_e64 v162, v194, v172
	v_add_f32_e64 v163, v195, v173
	v_pk_add_f32 v[162:163], v[162:163], v[162:163] op_sel:[0,1] op_sel_hi:[1,0]
	v_mfma_f32_32x32x16_bf16 v[34:49], v[206:209], v[166:169], v[34:49]
	v_mfma_f32_32x32x16_bf16 v[18:33], v[210:213], v[166:169], v[18:33]
	ds_read_b128 v[194:197], v176 offset:20480
	ds_read_b128 v[198:201], v176 offset:21504
	ds_read_b128 v[202:205], v176 offset:22528
	ds_read_b128 v[206:209], v176 offset:23552
	ds_read_b128 v[210:213], v189 offset:57600
	ds_read_b128 v[214:217], v189 offset:57616
	ds_read_b128 v[222:225], v176 offset:24576
	ds_read_b128 v[226:229], v176 offset:25600
	ds_read_b128 v[230:233], v176 offset:26624
	ds_read_b128 v[234:237], v176 offset:27648
	ds_read_b128 v[238:241], v189 offset:57664
	ds_read_b128 v[242:245], v189 offset:57680
	v_mfma_f32_32x32x16_bf16 v[2:17], v[218:221], v[166:169], v[2:17]
	v_lshlrev_b32_e32 v166, 16, v158
	v_and_b32_e32 v167, 0xffff0000, v158
	v_lshlrev_b32_e32 v168, 16, v159
	v_and_b32_e32 v169, 0xffff0000, v159
	v_lshlrev_b32_e32 v158, 16, v160
	v_and_b32_e32 v159, 0xffff0000, v160
	v_lshlrev_b32_e32 v160, 16, v161
	v_and_b32_e32 v161, 0xffff0000, v161
	s_waitcnt lgkmcnt(0)
	v_pk_mul_f32 v[172:173], v[212:213], v[168:169]
	v_pk_mul_f32 v[218:219], v[210:211], v[166:167]
	v_pk_mul_f32 v[214:215], v[214:215], v[158:159]
	v_pk_mul_f32 v[216:217], v[216:217], v[160:161]
	v_cvt_pk_bf16_f32 v160, v214, v215
	v_cvt_pk_bf16_f32 v158, v218, v219
	v_cvt_pk_bf16_f32 v161, v216, v217
	v_cvt_pk_bf16_f32 v159, v172, v173
	v_pk_fma_f32 v[172:173], v[212:213], v[168:169], v[216:217]
	v_pk_fma_f32 v[218:219], v[210:211], v[166:167], v[214:215]
	v_mfma_f32_32x32x16_bf16 v[50:65], v[194:197], v[158:161], v[50:65]
	v_mfma_f32_32x32x16_bf16 v[34:49], v[198:201], v[158:161], v[34:49]
	v_mfma_f32_32x32x16_bf16 v[18:33], v[202:205], v[158:161], v[18:33]
	ds_read_b128 v[166:169], v176 offset:28672
	ds_read_b128 v[194:197], v176 offset:29696
	ds_read_b128 v[198:201], v176 offset:30720
	ds_read_b128 v[202:205], v176 offset:31744
	ds_read_b128 v[210:213], v189 offset:57728
	ds_read_b128 v[214:217], v189 offset:57744
	v_mfma_f32_32x32x16_bf16 v[2:17], v[206:209], v[158:161], v[2:17]
	v_lshlrev_b32_e32 v206, 16, v154
	v_and_b32_e32 v207, 0xffff0000, v154
	v_lshlrev_b32_e32 v154, 16, v155
	v_and_b32_e32 v155, 0xffff0000, v155
	v_lshlrev_b32_e32 v158, 16, v156
	v_and_b32_e32 v159, 0xffff0000, v156
	v_lshlrev_b32_e32 v156, 16, v157
	v_and_b32_e32 v157, 0xffff0000, v157
	v_pk_mul_f32 v[208:209], v[240:241], v[154:155]
	v_pk_mul_f32 v[220:221], v[238:239], v[206:207]
	v_pk_mul_f32 v[242:243], v[242:243], v[158:159]
	v_pk_mul_f32 v[156:157], v[244:245], v[156:157]
	v_cvt_pk_bf16_f32 v160, v242, v243
	v_cvt_pk_bf16_f32 v158, v220, v221
	v_cvt_pk_bf16_f32 v161, v156, v157
	v_cvt_pk_bf16_f32 v159, v208, v209
	v_pk_fma_f32 v[154:155], v[240:241], v[154:155], v[156:157]
	v_pk_fma_f32 v[156:157], v[238:239], v[206:207], v[242:243]
	v_mfma_f32_32x32x16_bf16 v[50:65], v[222:225], v[158:161], v[50:65]
	v_add_f32_e64 v156, v218, v156
	v_add_f32_e64 v157, v219, v157
	v_add_f32_e64 v154, v172, v154
	v_add_f32_e64 v155, v173, v155
	v_pk_mov_b32 v[172:173], v[156:157], v[154:155] op_sel:[1,0]
	v_mov_b32_e32 v157, v155
	v_pk_add_f32 v[154:155], v[172:173], v[156:157]
	v_mfma_f32_32x32x16_bf16 v[34:49], v[226:229], v[158:161], v[34:49]
	v_add_f32_e64 v156, v154, v155
	v_add_f32_e64 v157, v155, v154
	v_mfma_f32_32x32x16_bf16 v[18:33], v[230:233], v[158:161], v[18:33]
	ds_read_b128 v[206:209], v176 offset:32768
	ds_read_b128 v[218:221], v176 offset:33792
	ds_read_b128 v[222:225], v176 offset:34816
	ds_read_b128 v[226:229], v176 offset:35840
	ds_read_b128 v[230:233], v189 offset:57792
	ds_read_b128 v[238:241], v189 offset:57808
	v_mfma_f32_32x32x16_bf16 v[2:17], v[234:237], v[158:161], v[2:17]
	v_lshlrev_b32_e32 v154, 16, v150
	v_and_b32_e32 v155, 0xffff0000, v150
	v_lshlrev_b32_e32 v158, 16, v151
	v_and_b32_e32 v159, 0xffff0000, v151
	v_lshlrev_b32_e32 v150, 16, v152
	v_and_b32_e32 v151, 0xffff0000, v152
	v_lshlrev_b32_e32 v152, 16, v153
	v_and_b32_e32 v153, 0xffff0000, v153
	s_waitcnt lgkmcnt(0)
	v_pk_mul_f32 v[160:161], v[212:213], v[158:159]
	v_pk_mul_f32 v[172:173], v[210:211], v[154:155]
	v_pk_mul_f32 v[214:215], v[214:215], v[150:151]
	v_pk_mul_f32 v[216:217], v[216:217], v[152:153]
	v_cvt_pk_bf16_f32 v152, v214, v215
	v_cvt_pk_bf16_f32 v150, v172, v173
	v_cvt_pk_bf16_f32 v153, v216, v217
	v_cvt_pk_bf16_f32 v151, v160, v161
	v_pk_fma_f32 v[158:159], v[212:213], v[158:159], v[216:217]
	v_pk_fma_f32 v[154:155], v[210:211], v[154:155], v[214:215]
	v_mfma_f32_32x32x16_bf16 v[50:65], v[166:169], v[150:153], v[50:65]
	v_mfma_f32_32x32x16_bf16 v[34:49], v[194:197], v[150:153], v[34:49]
	v_mfma_f32_32x32x16_bf16 v[18:33], v[198:201], v[150:153], v[18:33]
	v_mfma_f32_32x32x16_bf16 v[2:17], v[202:205], v[150:153], v[2:17]
	v_lshlrev_b32_e32 v152, 16, v146
	v_and_b32_e32 v153, 0xffff0000, v146
	v_lshlrev_b32_e32 v146, 16, v147
	v_and_b32_e32 v147, 0xffff0000, v147
	v_mov_b32_e32 v157, 0x5000
	v_lshlrev_b32_e32 v150, 16, v148
	v_and_b32_e32 v151, 0xffff0000, v148
	v_lshlrev_b32_e32 v148, 16, v149
	v_and_b32_e32 v149, 0xffff0000, v149
	v_pk_mul_f32 v[160:161], v[232:233], v[146:147]
	s_mov_b64 s[2:3], 0x5000
	v_mad_u32_u24 v157, v192, s1, v157
	v_pk_mul_f32 v[172:173], v[240:241], v[148:149]
	v_cvt_pk_bf16_f32 v149, v160, v161
	v_lshl_add_u64 v[160:161], v[164:165], 0, s[2:3]
	v_readfirstlane_b32 s2, v157
	s_mov_b32 m0, s2
	v_mov_b32_e32 v157, 0x6000
	s_waitcnt lgkmcnt(0)
	s_barrier
	global_load_lds_dwordx4 v[160:161], off
	global_load_lds_dwordx4 v[160:161], off offset:1024
	global_load_lds_dwordx4 v[160:161], off offset:2048
	global_load_lds_dwordx4 v[160:161], off offset:3072
	v_mad_u32_u24 v157, v192, s1, v157
	s_mov_b64 s[2:3], 0x6000
	v_readfirstlane_b32 s1, v157
	v_lshl_add_u64 v[160:161], v[164:165], 0, s[2:3]
	s_mov_b32 m0, s1
	v_pk_mul_f32 v[168:169], v[238:239], v[150:151]
	global_load_lds_dwordx4 v[160:161], off
	v_pk_mul_f32 v[166:167], v[230:231], v[152:153]
	v_pk_fma_f32 v[146:147], v[232:233], v[146:147], v[172:173]
	v_pk_fma_f32 v[152:153], v[230:231], v[152:153], v[168:169]
	v_pk_add_f32 v[146:147], v[158:159], v[146:147]
	v_pk_add_f32 v[152:153], v[154:155], v[152:153]
	v_cvt_pk_bf16_f32 v150, v168, v169
	v_cvt_pk_bf16_f32 v148, v166, v167
	v_cvt_pk_bf16_f32 v151, v172, v173
	v_pk_mov_b32 v[154:155], v[152:153], v[146:147] op_sel:[1,0]
	v_mov_b32_e32 v153, v147
	v_mfma_f32_32x32x16_bf16 v[50:65], v[206:209], v[148:151], v[50:65]
	v_add_f32_e64 v146, v154, v152
	v_add_f32_e64 v147, v155, v153
	v_pk_add_f32 v[146:147], v[146:147], v[146:147] op_sel:[0,1] op_sel_hi:[1,0]
	v_mfma_f32_32x32x16_bf16 v[34:49], v[218:221], v[148:151], v[34:49]
	v_mfma_f32_32x32x16_bf16 v[18:33], v[222:225], v[148:151], v[18:33]
	ds_read_b128 v[152:155], v176 offset:40960
	ds_read_b128 v[158:161], v176 offset:41984
	ds_read_b128 v[164:167], v176 offset:43008
	ds_read_b128 v[194:197], v176 offset:44032
	ds_read_b128 v[198:201], v189 offset:57856
	ds_read_b128 v[202:205], v189 offset:57872
	ds_read_b128 v[206:209], v176 offset:45056
	ds_read_b128 v[210:213], v176 offset:46080
	ds_read_b128 v[214:217], v176 offset:47104
	ds_read_b128 v[218:221], v176 offset:48128
	ds_read_b128 v[222:225], v189 offset:57920
	ds_read_b128 v[230:233], v189 offset:57936
	v_mfma_f32_32x32x16_bf16 v[2:17], v[226:229], v[148:151], v[2:17]
	v_lshlrev_b32_e32 v148, 16, v110
	v_and_b32_e32 v149, 0xffff0000, v110
	v_lshlrev_b32_e32 v150, 16, v111
	v_and_b32_e32 v151, 0xffff0000, v111
	v_lshlrev_b32_e32 v110, 16, v112
	v_and_b32_e32 v111, 0xffff0000, v112
	v_lshlrev_b32_e32 v112, 16, v113
	v_and_b32_e32 v113, 0xffff0000, v113
	s_waitcnt lgkmcnt(0)
	v_pk_mul_f32 v[168:169], v[200:201], v[150:151]
	v_pk_mul_f32 v[172:173], v[198:199], v[148:149]
	v_pk_mul_f32 v[202:203], v[202:203], v[110:111]
	v_pk_mul_f32 v[204:205], v[204:205], v[112:113]
	v_cvt_pk_bf16_f32 v112, v202, v203
	v_cvt_pk_bf16_f32 v110, v172, v173
	v_cvt_pk_bf16_f32 v113, v204, v205
	v_cvt_pk_bf16_f32 v111, v168, v169
	v_pk_fma_f32 v[148:149], v[198:199], v[148:149], v[202:203]
	s_nop 0
	v_mfma_f32_32x32x16_bf16 v[50:65], v[152:155], v[110:113], v[50:65]
	v_fma_f32 v154, v200, v150, v204
	v_fma_f32 v155, v201, v151, v205
	v_mfma_f32_32x32x16_bf16 v[34:49], v[158:161], v[110:113], v[34:49]
	v_mfma_f32_32x32x16_bf16 v[18:33], v[164:167], v[110:113], v[18:33]
	ds_read_b128 v[150:153], v176 offset:49152
	ds_read_b128 v[158:161], v176 offset:50176
	ds_read_b128 v[164:167], v176 offset:51200
	ds_read_b128 v[198:201], v176 offset:52224
	ds_read_b128 v[202:205], v189 offset:57984
	ds_read_b128 v[226:229], v189 offset:58000
	v_mfma_f32_32x32x16_bf16 v[2:17], v[194:197], v[110:113], v[2:17]
	v_lshlrev_b32_e32 v110, 16, v90
	v_and_b32_e32 v111, 0xffff0000, v90
	v_lshlrev_b32_e32 v112, 16, v91
	v_and_b32_e32 v113, 0xffff0000, v91
	v_lshlrev_b32_e32 v90, 16, v92
	v_and_b32_e32 v91, 0xffff0000, v92
	v_lshlrev_b32_e32 v92, 16, v93
	v_and_b32_e32 v93, 0xffff0000, v93
	v_pk_mul_f32 v[194:195], v[230:231], v[90:91]
	v_pk_mul_f32 v[196:197], v[232:233], v[92:93]
	v_pk_mul_f32 v[168:169], v[224:225], v[112:113]
	v_pk_mul_f32 v[172:173], v[222:223], v[110:111]
	v_pk_fma_f32 v[112:113], v[224:225], v[112:113], v[196:197]
	v_pk_fma_f32 v[110:111], v[222:223], v[110:111], v[194:195]
	v_pk_add_f32 v[112:113], v[154:155], v[112:113]
	v_pk_add_f32 v[110:111], v[148:149], v[110:111]
	v_cvt_pk_bf16_f32 v92, v194, v195
	v_pk_mov_b32 v[148:149], v[110:111], v[112:113] op_sel:[1,0]
	v_mov_b32_e32 v111, v113
	v_cvt_pk_bf16_f32 v90, v172, v173
	v_cvt_pk_bf16_f32 v93, v196, v197
	v_cvt_pk_bf16_f32 v91, v168, v169
	v_pk_add_f32 v[110:111], v[148:149], v[110:111]
	s_nop 0
	v_mfma_f32_32x32x16_bf16 v[50:65], v[206:209], v[90:93], v[50:65]
	v_add_f32_e64 v148, v110, v111
	v_add_f32_e64 v149, v111, v110
	v_mfma_f32_32x32x16_bf16 v[34:49], v[210:213], v[90:93], v[34:49]
	v_mfma_f32_32x32x16_bf16 v[18:33], v[214:217], v[90:93], v[18:33]
	ds_read_b128 v[110:113], v176 offset:53248
	ds_read_b128 v[194:197], v176 offset:54272
	ds_read_b128 v[206:209], v176 offset:55296
	ds_read_b128 v[210:213], v176 offset:56320
	ds_read_b128 v[214:217], v189 offset:58048
	ds_read_b128 v[222:225], v189 offset:58064
	v_mfma_f32_32x32x16_bf16 v[2:17], v[218:221], v[90:93], v[2:17]
	v_lshlrev_b32_e32 v90, 16, v86
	v_and_b32_e32 v91, 0xffff0000, v86
	v_lshlrev_b32_e32 v92, 16, v87
	v_and_b32_e32 v93, 0xffff0000, v87
	v_lshlrev_b32_e32 v86, 16, v88
	v_and_b32_e32 v87, 0xffff0000, v88
	v_lshlrev_b32_e32 v88, 16, v89
	v_and_b32_e32 v89, 0xffff0000, v89
	s_waitcnt lgkmcnt(0)
	v_pk_mul_f32 v[154:155], v[204:205], v[92:93]
	v_pk_mul_f32 v[168:169], v[202:203], v[90:91]
	v_pk_mul_f32 v[172:173], v[226:227], v[86:87]
	v_pk_mul_f32 v[218:219], v[228:229], v[88:89]
	v_cvt_pk_bf16_f32 v88, v172, v173
	v_cvt_pk_bf16_f32 v86, v168, v169
	v_cvt_pk_bf16_f32 v89, v218, v219
	v_cvt_pk_bf16_f32 v87, v154, v155
	v_pk_fma_f32 v[92:93], v[204:205], v[92:93], v[218:219]
	v_pk_fma_f32 v[90:91], v[202:203], v[90:91], v[172:173]
	v_mfma_f32_32x32x16_bf16 v[50:65], v[150:153], v[86:89], v[50:65]
	v_mfma_f32_32x32x16_bf16 v[34:49], v[158:161], v[86:89], v[34:49]
	v_mfma_f32_32x32x16_bf16 v[18:33], v[164:167], v[86:89], v[18:33]
	v_mfma_f32_32x32x16_bf16 v[2:17], v[198:201], v[86:89], v[2:17]
	v_lshlrev_b32_e32 v86, 16, v82
	v_and_b32_e32 v87, 0xffff0000, v82
	v_lshlrev_b32_e32 v88, 16, v83
	v_and_b32_e32 v89, 0xffff0000, v83
	v_lshlrev_b32_e32 v82, 16, v84
	v_and_b32_e32 v83, 0xffff0000, v84
	v_lshlrev_b32_e32 v84, 16, v85
	v_and_b32_e32 v85, 0xffff0000, v85
	v_pk_mul_f32 v[150:151], v[216:217], v[88:89]
	v_pk_mul_f32 v[152:153], v[214:215], v[86:87]
	v_pk_mul_f32 v[154:155], v[222:223], v[82:83]
	v_pk_mul_f32 v[158:159], v[224:225], v[84:85]
	v_cvt_pk_bf16_f32 v84, v154, v155
	v_cvt_pk_bf16_f32 v82, v152, v153
	v_cvt_pk_bf16_f32 v85, v158, v159
	v_cvt_pk_bf16_f32 v83, v150, v151
	v_pk_fma_f32 v[88:89], v[216:217], v[88:89], v[158:159]
	v_pk_fma_f32 v[86:87], v[214:215], v[86:87], v[154:155]
	s_mov_b64 s[2:3], 0x3000
	v_mfma_f32_32x32x16_bf16 v[50:65], v[110:113], v[82:85], v[50:65]
	v_add_f32_e64 v86, v90, v86
	v_add_f32_e64 v87, v91, v87
	v_add_f32_e64 v88, v92, v88
	v_add_f32_e64 v89, v93, v89
	s_waitcnt vmcnt(5)
	v_pk_mov_b32 v[90:91], v[86:87], v[88:89] op_sel:[1,0]
	v_mov_b32_e32 v87, v89
	v_pk_add_f32 v[86:87], v[90:91], v[86:87]
	v_lshrrev_b32_e32 v161, 3, v191
	v_mfma_f32_32x32x16_bf16 v[34:49], v[194:197], v[82:85], v[34:49]
	s_movk_i32 s1, 0x90
	v_or_b32_e32 v152, v1, v174
	v_add_f32_e64 v150, v86, v87
	v_add_f32_e64 v151, v87, v86
	v_mad_u32_u24 v155, v161, s1, v152
	v_mul_u32_u24_e32 v147, 0x90, v188
	v_mad_u32_u24 v149, v192, s0, v147
	v_and_b32_e32 v147, 32, v0
	v_mfma_f32_32x32x16_bf16 v[18:33], v[206:209], v[82:85], v[18:33]
	v_add_u32_e32 v151, v149, v147
	v_lshrrev_b32_e32 v147, 1, v191
	v_and_b32_e32 v154, 16, v147
	v_add_u32_e32 v160, v149, v154
	v_sub_u32_e32 v147, v189, v154
	s_mov_b64 s[8:9], 0x16000
	s_brev_b32 s0, 60
	v_mfma_f32_32x32x16_bf16 v[2:17], v[210:213], v[82:85], v[2:17]
	v_lshl_add_u64 v[82:83], v[184:185], 0, s[2:3]
	s_mov_b64 s[2:3], 0x3400
	global_load_dwordx4 v[110:113], v[82:83], off
	v_lshl_add_u64 v[82:83], v[184:185], 0, s[2:3]
	s_mov_b64 s[2:3], 0x3800
	global_load_dwordx4 v[90:93], v[82:83], off
	v_lshl_add_u64 v[82:83], v[184:185], 0, s[2:3]
	s_mov_b64 s[2:3], 0x3c00
	global_load_dwordx4 v[86:89], v[82:83], off
	v_lshl_add_u64 v[82:83], v[184:185], 0, s[2:3]
	global_load_dwordx4 v[82:85], v[82:83], off
	s_waitcnt lgkmcnt(0)
	s_barrier
	ds_write_b128 v155, v[142:145] offset:61440
	v_mov_b32_e32 v142, 0x480
	v_mad_u32_u24 v165, v161, s1, v142
	v_add_u32_e32 v157, v152, v165
	ds_write_b128 v157, v[134:137] offset:61440
	v_mov_b32_e32 v134, 0x900
	v_mad_u32_u24 v164, v161, s1, v134
	v_add_u32_e32 v171, v152, v164
	ds_write_b128 v171, v[130:133] offset:61440
	v_mov_b32_e32 v130, 0xd80
	v_mad_u32_u24 v163, v161, s1, v130
	v_add_u32_e32 v174, v152, v163
	ds_write_b128 v174, v[138:141] offset:61440
	ds_read_b128 v[142:145], v151 offset:61440
	ds_read_b128 v[138:141], v151 offset:61456
	ds_read_b128 v[134:137], v151 offset:61504
	ds_read_b128 v[130:133], v151 offset:61520
	ds_read_b128 v[166:169], v160 offset:61440
	ds_read_b128 v[192:195], v160 offset:61472
	ds_read_b128 v[196:199], v147 offset:58368
	ds_read_b128 v[200:203], v147 offset:58400
	ds_read_b128 v[204:207], v160 offset:61504
	ds_read_b128 v[208:211], v160 offset:61536
	ds_read_b128 v[212:215], v147 offset:58432
	ds_read_b128 v[216:219], v147 offset:58464
	s_waitcnt lgkmcnt(0)
	v_pk_add_f32 v[152:153], v[168:169], v[198:199]
	v_pk_add_f32 v[158:159], v[166:167], v[196:197]
	v_pk_add_f32 v[166:167], v[194:195], v[202:203]
	v_pk_add_f32 v[168:169], v[192:193], v[200:201]
	v_pk_add_f32 v[192:193], v[210:211], v[218:219]
	v_pk_add_f32 v[194:195], v[208:209], v[216:217]
	v_pk_add_f32 v[172:173], v[206:207], v[214:215]
	v_pk_add_f32 v[184:185], v[204:205], v[212:213]
	v_pk_add_f32 v[62:63], v[194:195], v[62:63]
	v_pk_add_f32 v[54:55], v[168:169], v[54:55]
	v_pk_add_f32 v[64:65], v[192:193], v[64:65]
	v_pk_add_f32 v[56:57], v[166:167], v[56:57]
	ds_write_b128 v155, v[114:117] offset:61440
	ds_write_b128 v157, v[118:121] offset:61440
	ds_write_b128 v171, v[122:125] offset:61440
	ds_write_b128 v174, v[126:129] offset:61440
	ds_read_b128 v[126:129], v151 offset:61440
	ds_read_b128 v[122:125], v151 offset:61456
	ds_read_b128 v[118:121], v151 offset:61504
	ds_read_b128 v[114:117], v151 offset:61520
	ds_read_b128 v[166:169], v160 offset:61440
	ds_read_b128 v[192:195], v160 offset:61472
	ds_read_b128 v[196:199], v147 offset:58496
	ds_read_b128 v[200:203], v147 offset:58528
	ds_read_b128 v[204:207], v160 offset:61504
	ds_read_b128 v[208:211], v160 offset:61536
	ds_read_b128 v[212:215], v147 offset:58560
	ds_read_b128 v[216:219], v147 offset:58592
	v_pk_add_f32 v[52:53], v[152:153], v[52:53]
	v_pk_add_f32 v[50:51], v[158:159], v[50:51]
	s_waitcnt lgkmcnt(0)
	v_pk_add_f32 v[152:153], v[168:169], v[198:199]
	v_pk_add_f32 v[158:159], v[166:167], v[196:197]
	v_pk_add_f32 v[166:167], v[194:195], v[202:203]
	v_pk_add_f32 v[168:169], v[192:193], v[200:201]
	v_pk_add_f32 v[192:193], v[210:211], v[218:219]
	v_pk_add_f32 v[194:195], v[208:209], v[216:217]
	v_pk_add_f32 v[58:59], v[184:185], v[58:59]
	v_pk_add_f32 v[60:61], v[172:173], v[60:61]
	v_pk_add_f32 v[172:173], v[206:207], v[214:215]
	v_pk_add_f32 v[184:185], v[204:205], v[212:213]
	v_pk_add_f32 v[46:47], v[194:195], v[46:47]
	v_pk_add_f32 v[38:39], v[168:169], v[38:39]
	v_pk_add_f32 v[48:49], v[192:193], v[48:49]
	v_pk_add_f32 v[40:41], v[166:167], v[40:41]
	ds_write_b128 v155, v[102:105] offset:61440
	ds_write_b128 v157, v[94:97] offset:61440
	ds_write_b128 v171, v[98:101] offset:61440
	ds_write_b128 v174, v[106:109] offset:61440
	ds_read_b128 v[106:109], v151 offset:61440
	ds_read_b128 v[102:105], v151 offset:61456
	ds_read_b128 v[98:101], v151 offset:61504
	ds_read_b128 v[94:97], v151 offset:61520
	ds_read_b128 v[166:169], v160 offset:61440
	ds_read_b128 v[192:195], v160 offset:61472
	ds_read_b128 v[196:199], v147 offset:58624
	ds_read_b128 v[200:203], v147 offset:58656
	ds_read_b128 v[204:207], v160 offset:61504
	ds_read_b128 v[208:211], v160 offset:61536
	ds_read_b128 v[212:215], v147 offset:58688
	ds_read_b128 v[216:219], v147 offset:58720
	v_pk_add_f32 v[36:37], v[152:153], v[36:37]
	v_pk_add_f32 v[34:35], v[158:159], v[34:35]
	s_waitcnt lgkmcnt(0)
	v_pk_add_f32 v[152:153], v[168:169], v[198:199]
	v_pk_add_f32 v[158:159], v[166:167], v[196:197]
	v_pk_add_f32 v[166:167], v[194:195], v[202:203]
	v_pk_add_f32 v[168:169], v[192:193], v[200:201]
	v_pk_add_f32 v[192:193], v[210:211], v[218:219]
	v_pk_add_f32 v[194:195], v[208:209], v[216:217]
	v_add_f32_e32 v149, 0, v142
	v_pk_add_f32 v[42:43], v[184:185], v[42:43]
	v_pk_add_f32 v[44:45], v[172:173], v[44:45]
	v_pk_add_f32 v[172:173], v[206:207], v[214:215]
	v_pk_add_f32 v[184:185], v[204:205], v[212:213]
	v_pk_add_f32 v[30:31], v[194:195], v[30:31]
	v_pk_add_f32 v[22:23], v[168:169], v[22:23]
	v_pk_add_f32 v[32:33], v[192:193], v[32:33]
	v_pk_add_f32 v[24:25], v[166:167], v[24:25]
	ds_write_b128 v155, v[66:69] offset:61440
	ds_write_b128 v157, v[70:73] offset:61440
	ds_write_b128 v171, v[74:77] offset:61440
	ds_write_b128 v174, v[78:81] offset:61440
	ds_read_b128 v[78:81], v151 offset:61440
	ds_read_b128 v[74:77], v151 offset:61456
	ds_read_b128 v[70:73], v151 offset:61504
	ds_read_b128 v[66:69], v151 offset:61520
	ds_read_b128 v[166:169], v160 offset:61440
	ds_read_b128 v[192:195], v160 offset:61472
	ds_read_b128 v[196:199], v147 offset:58752
	ds_read_b128 v[200:203], v147 offset:58784
	ds_read_b128 v[204:207], v160 offset:61504
	ds_read_b128 v[208:211], v160 offset:61536
	ds_read_b128 v[212:215], v147 offset:58816
	ds_read_b128 v[216:219], v147 offset:58848
	v_add_f32_e32 v149, v149, v143
	v_mul_f32_e32 v151, v143, v143
	v_fmac_f32_e32 v151, v142, v142
	v_add_f32_e32 v149, v149, v144
	v_fmac_f32_e32 v151, v144, v144
	v_add_f32_e32 v149, v149, v145
	v_fmac_f32_e32 v151, v145, v145
	v_add_f32_e32 v149, v149, v138
	v_fmac_f32_e32 v151, v138, v138
	v_add_f32_e32 v149, v149, v139
	v_fmac_f32_e32 v151, v139, v139
	v_add_f32_e32 v149, v149, v140
	v_fmac_f32_e32 v151, v140, v140
	v_add_f32_e32 v149, v149, v141
	v_fmac_f32_e32 v151, v141, v141
	v_add_f32_e32 v149, v149, v134
	v_fmac_f32_e32 v151, v134, v134
	v_add_f32_e32 v149, v149, v135
	v_fmac_f32_e32 v151, v135, v135
	v_add_f32_e32 v149, v149, v136
	v_fmac_f32_e32 v151, v136, v136
	v_add_f32_e32 v149, v149, v137
	v_fmac_f32_e32 v151, v137, v137
	v_add_f32_e32 v149, v149, v130
	v_fmac_f32_e32 v151, v130, v130
	v_add_f32_e32 v149, v149, v131
	v_fmac_f32_e32 v151, v131, v131
	v_add_f32_e32 v149, v149, v132
	v_fmac_f32_e32 v151, v132, v132
	v_add_f32_e32 v149, v149, v133
	v_fmac_f32_e32 v151, v133, v133
	v_add_f32_e32 v149, v149, v126
	v_fmac_f32_e32 v151, v126, v126
	v_add_f32_e32 v149, v149, v127
	v_fmac_f32_e32 v151, v127, v127
	v_add_f32_e32 v149, v149, v128
	v_fmac_f32_e32 v151, v128, v128
	v_add_f32_e32 v149, v149, v129
	v_fmac_f32_e32 v151, v129, v129
	v_add_f32_e32 v149, v149, v122
	v_fmac_f32_e32 v151, v122, v122
	v_add_f32_e32 v149, v149, v123
	v_fmac_f32_e32 v151, v123, v123
	v_add_f32_e32 v149, v149, v124
	v_fmac_f32_e32 v151, v124, v124
	v_add_f32_e32 v149, v149, v125
	v_fmac_f32_e32 v151, v125, v125
	v_add_f32_e32 v149, v149, v118
	v_fmac_f32_e32 v151, v118, v118
	v_add_f32_e32 v149, v149, v119
	v_fmac_f32_e32 v151, v119, v119
	v_add_f32_e32 v149, v149, v120
	v_fmac_f32_e32 v151, v120, v120
	v_add_f32_e32 v149, v149, v121
	v_fmac_f32_e32 v151, v121, v121
	v_add_f32_e32 v149, v149, v114
	v_fmac_f32_e32 v151, v114, v114
	v_add_f32_e32 v149, v149, v115
	v_fmac_f32_e32 v151, v115, v115
	v_add_f32_e32 v149, v149, v116
	v_fmac_f32_e32 v151, v116, v116
	v_add_f32_e32 v149, v149, v117
	v_fmac_f32_e32 v151, v117, v117
	v_add_f32_e32 v149, v149, v106
	v_fmac_f32_e32 v151, v106, v106
	v_add_f32_e32 v149, v149, v107
	v_fmac_f32_e32 v151, v107, v107
	v_add_f32_e32 v149, v149, v108
	v_fmac_f32_e32 v151, v108, v108
	v_add_f32_e32 v149, v149, v109
	v_fmac_f32_e32 v151, v109, v109
	v_add_f32_e32 v149, v149, v102
	v_fmac_f32_e32 v151, v102, v102
	v_add_f32_e32 v149, v149, v103
	v_fmac_f32_e32 v151, v103, v103
	v_add_f32_e32 v149, v149, v104
	v_fmac_f32_e32 v151, v104, v104
	v_add_f32_e32 v149, v149, v105
	v_fmac_f32_e32 v151, v105, v105
	v_add_f32_e32 v149, v149, v98
	v_fmac_f32_e32 v151, v98, v98
	v_add_f32_e32 v149, v149, v99
	v_fmac_f32_e32 v151, v99, v99
	v_add_f32_e32 v149, v149, v100
	v_fmac_f32_e32 v151, v100, v100
	v_add_f32_e32 v149, v149, v101
	v_fmac_f32_e32 v151, v101, v101
	v_add_f32_e32 v149, v149, v94
	v_fmac_f32_e32 v151, v94, v94
	v_add_f32_e32 v149, v149, v95
	v_fmac_f32_e32 v151, v95, v95
	v_add_f32_e32 v149, v149, v96
	v_fmac_f32_e32 v151, v96, v96
	v_add_f32_e32 v149, v149, v97
	v_fmac_f32_e32 v151, v97, v97
	s_waitcnt lgkmcnt(0)
	v_add_f32_e32 v149, v149, v78
	v_fmac_f32_e32 v151, v78, v78
	v_add_f32_e32 v149, v149, v79
	v_fmac_f32_e32 v151, v79, v79
	v_add_f32_e32 v149, v149, v80
	v_fmac_f32_e32 v151, v80, v80
	v_add_f32_e32 v149, v149, v81
	v_fmac_f32_e32 v151, v81, v81
	v_add_f32_e32 v149, v149, v74
	v_fmac_f32_e32 v151, v74, v74
	v_add_f32_e32 v149, v149, v75
	v_fmac_f32_e32 v151, v75, v75
	v_add_f32_e32 v149, v149, v76
	v_pk_add_f32 v[20:21], v[152:153], v[20:21]
	v_pk_add_f32 v[152:153], v[168:169], v[198:199]
	v_pk_add_f32 v[168:169], v[192:193], v[200:201]
	v_fmac_f32_e32 v151, v76, v76
	v_add_f32_e32 v149, v149, v77
	v_pk_add_f32 v[6:7], v[168:169], v[6:7]
	v_fmac_f32_e32 v151, v77, v77
	v_add_f32_e32 v149, v149, v70
	v_pk_mul_f32 v[168:169], v[70:71], v[70:71]
	v_pk_add_f32 v[18:19], v[158:159], v[18:19]
	v_pk_add_f32 v[158:159], v[166:167], v[196:197]
	v_pk_add_f32 v[166:167], v[194:195], v[202:203]
	v_add_f32_e32 v149, v149, v71
	v_add_f32_e32 v151, v151, v168
	v_pk_add_f32 v[8:9], v[166:167], v[8:9]
	v_pk_mul_f32 v[166:167], v[72:73], v[72:73]
	v_add_f32_e32 v151, v151, v169
	v_add_f32_e32 v149, v149, v72
	v_add_f32_e32 v149, v149, v73
	v_add_f32_e32 v151, v151, v166
	v_add_f32_e32 v151, v151, v167
	v_add_f32_e32 v149, v149, v66
	v_pk_mul_f32 v[168:169], v[66:67], v[66:67]
	v_add_f32_e32 v149, v149, v67
	v_add_f32_e32 v151, v151, v168
	v_pk_mul_f32 v[166:167], v[68:69], v[68:69]
	v_add_f32_e32 v151, v151, v169
	v_add_f32_e32 v149, v149, v68
	v_add_f32_e32 v169, v149, v69
	v_add_f32_e32 v149, v151, v166
	v_add_f32_e32 v168, v149, v167
	v_mov_b32_e32 v167, v169
	v_mov_b32_e32 v166, v168
	s_nop 0
	v_permlane32_swap_b32_e32 v169, v167
	v_permlane32_swap_b32_e32 v168, v166
	v_readfirstlane_b32 s3, v187
	v_pk_add_f32 v[166:167], v[168:169], v[166:167]
	v_lshl_add_u64 v[168:169], v[180:181], 0, s[8:9]
	s_mov_b32 m0, s3
	s_nop 0
	global_load_lds_dwordx4 v[168:169], off
	global_load_lds_dwordx4 v[168:169], off offset:1024
	global_load_lds_dwordx4 v[168:169], off offset:2048
	global_load_lds_dwordx4 v[168:169], off offset:3072
	v_pk_mul_f32 v[166:167], v[166:167], s[0:1] op_sel_hi:[1,0]
	s_mov_b32 s2, 0x800000
	v_fma_f32 v149, -v167, v167, v166
	v_add_f32_e32 v149, 0x3727c5ac, v149
	v_mul_f32_e32 v151, 0x4b800000, v149
	v_cmp_gt_f32_e32 vcc, s2, v149
	v_pk_add_f32 v[4:5], v[152:153], v[4:5]
	v_pk_add_f32 v[2:3], v[158:159], v[2:3]
	v_cndmask_b32_e32 v149, v149, v151, vcc
	v_rsq_f32_e32 v149, v149
	v_pk_add_f32 v[26:27], v[184:185], v[26:27]
	v_pk_add_f32 v[28:29], v[172:173], v[28:29]
	v_pk_add_f32 v[172:173], v[206:207], v[214:215]
	v_mul_f32_e32 v151, 0x45800000, v149
	v_cndmask_b32_e32 v152, v149, v151, vcc
	v_mul_f32_e64 v158, v152, -v167
	v_pk_add_f32 v[184:185], v[204:205], v[212:213]
	v_pk_add_f32 v[192:193], v[210:211], v[218:219]
	v_pk_add_f32 v[194:195], v[208:209], v[216:217]
	v_pk_fma_f32 v[142:143], v[152:153], v[142:143], v[158:159] op_sel_hi:[0,1,0]
	v_pk_fma_f32 v[144:145], v[152:153], v[144:145], v[158:159] op_sel_hi:[0,1,0]
	v_pk_fma_f32 v[138:139], v[152:153], v[138:139], v[158:159] op_sel_hi:[0,1,0]
	v_pk_fma_f32 v[140:141], v[152:153], v[140:141], v[158:159] op_sel_hi:[0,1,0]
	v_pk_fma_f32 v[134:135], v[152:153], v[134:135], v[158:159] op_sel_hi:[0,1,0]
	v_pk_fma_f32 v[136:137], v[152:153], v[136:137], v[158:159] op_sel_hi:[0,1,0]
	v_pk_fma_f32 v[130:131], v[152:153], v[130:131], v[158:159] op_sel_hi:[0,1,0]
	v_pk_fma_f32 v[132:133], v[152:153], v[132:133], v[158:159] op_sel_hi:[0,1,0]
	v_pk_fma_f32 v[126:127], v[152:153], v[126:127], v[158:159] op_sel_hi:[0,1,0]
	v_pk_fma_f32 v[128:129], v[152:153], v[128:129], v[158:159] op_sel_hi:[0,1,0]
	v_pk_fma_f32 v[122:123], v[152:153], v[122:123], v[158:159] op_sel_hi:[0,1,0]
	v_pk_fma_f32 v[124:125], v[152:153], v[124:125], v[158:159] op_sel_hi:[0,1,0]
	v_pk_fma_f32 v[118:119], v[152:153], v[118:119], v[158:159] op_sel_hi:[0,1,0]
	v_pk_fma_f32 v[120:121], v[152:153], v[120:121], v[158:159] op_sel_hi:[0,1,0]
	v_pk_fma_f32 v[114:115], v[152:153], v[114:115], v[158:159] op_sel_hi:[0,1,0]
	v_pk_fma_f32 v[116:117], v[152:153], v[116:117], v[158:159] op_sel_hi:[0,1,0]
	v_pk_fma_f32 v[106:107], v[152:153], v[106:107], v[158:159] op_sel_hi:[0,1,0]
	v_pk_fma_f32 v[108:109], v[152:153], v[108:109], v[158:159] op_sel_hi:[0,1,0]
	v_pk_fma_f32 v[102:103], v[152:153], v[102:103], v[158:159] op_sel_hi:[0,1,0]
	v_pk_fma_f32 v[104:105], v[152:153], v[104:105], v[158:159] op_sel_hi:[0,1,0]
	v_pk_fma_f32 v[98:99], v[152:153], v[98:99], v[158:159] op_sel_hi:[0,1,0]
	v_pk_fma_f32 v[100:101], v[152:153], v[100:101], v[158:159] op_sel_hi:[0,1,0]
	v_pk_fma_f32 v[94:95], v[152:153], v[94:95], v[158:159] op_sel_hi:[0,1,0]
	v_pk_fma_f32 v[96:97], v[152:153], v[96:97], v[158:159] op_sel_hi:[0,1,0]
	v_pk_fma_f32 v[78:79], v[152:153], v[78:79], v[158:159] op_sel_hi:[0,1,0]
	v_pk_fma_f32 v[80:81], v[152:153], v[80:81], v[158:159] op_sel_hi:[0,1,0]
	v_pk_fma_f32 v[74:75], v[152:153], v[74:75], v[158:159] op_sel_hi:[0,1,0]
	v_pk_fma_f32 v[76:77], v[152:153], v[76:77], v[158:159] op_sel_hi:[0,1,0]
	v_pk_add_f32 v[14:15], v[194:195], v[14:15]
	v_pk_add_f32 v[10:11], v[184:185], v[10:11]
	v_pk_add_f32 v[16:17], v[192:193], v[16:17]
	v_pk_add_f32 v[12:13], v[172:173], v[12:13]
	v_cvt_pk_bf16_f32 v141, v140, v141
	v_cvt_pk_bf16_f32 v140, v138, v139
	v_cvt_pk_bf16_f32 v139, v144, v145
	v_cvt_pk_bf16_f32 v138, v142, v143
	v_cvt_pk_bf16_f32 v133, v132, v133
	v_cvt_pk_bf16_f32 v132, v130, v131
	v_cvt_pk_bf16_f32 v131, v136, v137
	v_cvt_pk_bf16_f32 v130, v134, v135
	v_cvt_pk_bf16_f32 v125, v124, v125
	v_cvt_pk_bf16_f32 v124, v122, v123
	v_cvt_pk_bf16_f32 v123, v128, v129
	v_cvt_pk_bf16_f32 v122, v126, v127
	v_cvt_pk_bf16_f32 v117, v116, v117
	v_cvt_pk_bf16_f32 v116, v114, v115
	v_cvt_pk_bf16_f32 v115, v120, v121
	v_cvt_pk_bf16_f32 v114, v118, v119
	v_cvt_pk_bf16_f32 v105, v104, v105
	v_cvt_pk_bf16_f32 v104, v102, v103
	v_cvt_pk_bf16_f32 v103, v108, v109
	v_cvt_pk_bf16_f32 v102, v106, v107
	v_cvt_pk_bf16_f32 v109, v96, v97
	v_cvt_pk_bf16_f32 v108, v94, v95
	v_cvt_pk_bf16_f32 v107, v100, v101
	v_cvt_pk_bf16_f32 v106, v98, v99
	v_cvt_pk_bf16_f32 v121, v76, v77
	v_cvt_pk_bf16_f32 v120, v74, v75
	v_cvt_pk_bf16_f32 v119, v80, v81
	v_cvt_pk_bf16_f32 v118, v78, v79
	v_pk_fma_f32 v[172:173], v[152:153], v[70:71], v[158:159] op_sel_hi:[0,1,0]
	v_pk_fma_f32 v[94:95], v[152:153], v[72:73], v[158:159] op_sel_hi:[0,1,0]
	v_pk_fma_f32 v[184:185], v[152:153], v[66:67], v[158:159] op_sel_hi:[0,1,0]
	v_pk_fma_f32 v[96:97], v[152:153], v[68:69], v[158:159] op_sel_hi:[0,1,0]
	ds_read_b128 v[66:69], v176
	ds_read_b128 v[70:73], v176 offset:1024
	ds_read_b128 v[74:77], v176 offset:2048
	ds_read_b128 v[78:81], v176 offset:3072
	ds_read_b128 v[98:101], v176 offset:4096
	ds_read_b128 v[126:129], v176 offset:5120
	ds_read_b128 v[134:137], v176 offset:6144
	ds_read_b128 v[142:145], v176 offset:7168
	ds_read_b128 v[166:169], v176 offset:8192
	ds_read_b128 v[192:195], v176 offset:9216
	v_cvt_pk_bf16_f32 v97, v96, v97
	v_cvt_pk_bf16_f32 v96, v184, v185
	v_cvt_pk_bf16_f32 v95, v94, v95
	v_cvt_pk_bf16_f32 v94, v172, v173
	ds_read_b128 v[196:199], v176 offset:10240
	ds_read_b128 v[200:203], v176 offset:11264
	ds_read_b128 v[204:207], v176 offset:12288
	ds_read_b128 v[208:211], v176 offset:13312
	ds_read_b128 v[212:215], v176 offset:14336
	s_waitcnt lgkmcnt(0)
	v_mfma_f32_32x32x16_bf16 v[50:65], v[66:69], v[138:141], v[50:65]
	v_mfma_f32_32x32x16_bf16 v[34:49], v[70:73], v[138:141], v[34:49]
	v_mfma_f32_32x32x16_bf16 v[18:33], v[74:77], v[138:141], v[18:33]
	v_mfma_f32_32x32x16_bf16 v[2:17], v[78:81], v[138:141], v[2:17]
	v_mfma_f32_32x32x16_bf16 v[66:81], v[98:101], v[138:141], 0
	v_mfma_f32_32x32x16_bf16 v[50:65], v[126:129], v[130:133], v[50:65]
	v_mfma_f32_32x32x16_bf16 v[34:49], v[134:137], v[130:133], v[34:49]
	v_mfma_f32_32x32x16_bf16 v[18:33], v[142:145], v[130:133], v[18:33]
	ds_read_b128 v[98:101], v176 offset:15360
	ds_read_b128 v[126:129], v176 offset:16384
	ds_read_b128 v[134:137], v176 offset:17408
	ds_read_b128 v[138:141], v176 offset:18432
	ds_read_b128 v[142:145], v176 offset:19456
	v_mfma_f32_32x32x16_bf16 v[2:17], v[166:169], v[130:133], v[2:17]
	v_mfma_f32_32x32x16_bf16 v[66:81], v[192:195], v[130:133], v[66:81]
	v_mfma_f32_32x32x16_bf16 v[50:65], v[196:199], v[122:125], v[50:65]
	v_mfma_f32_32x32x16_bf16 v[34:49], v[200:203], v[122:125], v[34:49]
	v_mfma_f32_32x32x16_bf16 v[18:33], v[204:207], v[122:125], v[18:33]
	v_mfma_f32_32x32x16_bf16 v[2:17], v[208:211], v[122:125], v[2:17]
	v_mfma_f32_32x32x16_bf16 v[66:81], v[212:215], v[122:125], v[66:81]
	s_mov_b64 s[8:9], 0x1a000
	v_readfirstlane_b32 s3, v186
	s_waitcnt lgkmcnt(0)
	v_mfma_f32_32x32x16_bf16 v[50:65], v[98:101], v[114:117], v[50:65]
	v_lshl_add_u64 v[98:99], v[180:181], 0, s[8:9]
	s_mov_b32 m0, s3
	s_waitcnt vmcnt(8) lgkmcnt(0)
	s_barrier
	global_load_lds_dwordx4 v[98:99], off
	global_load_lds_dwordx4 v[98:99], off offset:1024
	global_load_lds_dwordx4 v[98:99], off offset:2048
	global_load_lds_dwordx4 v[98:99], off offset:3072
	v_mfma_f32_32x32x16_bf16 v[34:49], v[126:129], v[114:117], v[34:49]
	ds_read_b128 v[98:101], v176 offset:20480
	ds_read_b128 v[122:125], v176 offset:21504
	v_mfma_f32_32x32x16_bf16 v[18:33], v[134:137], v[114:117], v[18:33]
	v_mfma_f32_32x32x16_bf16 v[2:17], v[138:141], v[114:117], v[2:17]
	ds_read_b128 v[126:129], v176 offset:22528
	ds_read_b128 v[130:133], v176 offset:23552
	ds_read_b128 v[134:137], v176 offset:24576
	ds_read_b128 v[138:141], v176 offset:25600
	ds_read_b128 v[166:169], v176 offset:26624
	ds_read_b128 v[192:195], v176 offset:27648
	ds_read_b128 v[196:199], v176 offset:28672
	ds_read_b128 v[200:203], v176 offset:29696
	v_mfma_f32_32x32x16_bf16 v[66:81], v[142:145], v[114:117], v[66:81]
	s_waitcnt lgkmcnt(0)
	v_mfma_f32_32x32x16_bf16 v[34:49], v[122:125], v[102:105], v[34:49]
	v_mfma_f32_32x32x16_bf16 v[18:33], v[126:129], v[102:105], v[18:33]
	v_mfma_f32_32x32x16_bf16 v[2:17], v[130:133], v[102:105], v[2:17]
	ds_read_b128 v[114:117], v176 offset:31744
	ds_read_b128 v[122:125], v176 offset:32768
	ds_read_b128 v[126:129], v176 offset:33792
	ds_read_b128 v[130:133], v176 offset:30720
	ds_read_b128 v[142:145], v176 offset:34816
	v_mfma_f32_32x32x16_bf16 v[50:65], v[98:101], v[102:105], v[50:65]
	v_mfma_f32_32x32x16_bf16 v[66:81], v[134:137], v[102:105], v[66:81]
	v_mfma_f32_32x32x16_bf16 v[50:65], v[138:141], v[106:109], v[50:65]
	v_mfma_f32_32x32x16_bf16 v[34:49], v[166:169], v[106:109], v[34:49]
	ds_read_b128 v[102:105], v176 offset:35840
	ds_read_b128 v[134:137], v176 offset:36864
	ds_read_b128 v[138:141], v176 offset:37888
	ds_read_b128 v[166:169], v176 offset:38912
	ds_read_b128 v[98:101], v176 offset:39936
	v_mfma_f32_32x32x16_bf16 v[18:33], v[192:195], v[106:109], v[18:33]
	v_mfma_f32_32x32x16_bf16 v[2:17], v[196:199], v[106:109], v[2:17]
	v_mfma_f32_32x32x16_bf16 v[66:81], v[200:203], v[106:109], v[66:81]
	s_waitcnt lgkmcnt(0)
	v_mfma_f32_32x32x16_bf16 v[50:65], v[130:133], v[118:121], v[50:65]
	v_mfma_f32_32x32x16_bf16 v[34:49], v[114:117], v[118:121], v[34:49]
	v_mfma_f32_32x32x16_bf16 v[18:33], v[122:125], v[118:121], v[18:33]
	v_mfma_f32_32x32x16_bf16 v[2:17], v[126:129], v[118:121], v[2:17]
	v_mfma_f32_32x32x16_bf16 v[66:81], v[142:145], v[118:121], v[66:81]
	s_mov_b64 s[8:9], 0x1e000
	v_readfirstlane_b32 s3, v190
	v_mfma_f32_32x32x16_bf16 v[50:65], v[102:105], v[94:97], v[50:65]
	v_lshl_add_u64 v[102:103], v[180:181], 0, s[8:9]
	s_mov_b32 m0, s3
	s_waitcnt vmcnt(4) lgkmcnt(0)
	s_barrier
	global_load_lds_dwordx4 v[102:103], off
	global_load_lds_dwordx4 v[102:103], off offset:1024
	global_load_lds_dwordx4 v[102:103], off offset:2048
	global_load_lds_dwordx4 v[102:103], off offset:3072
	s_waitcnt vmcnt(4)
	v_mfma_f32_32x32x16_bf16 v[34:49], v[134:137], v[94:97], v[34:49]
	ds_read_b128 v[102:105], v176 offset:40960
	ds_read_b128 v[106:109], v176 offset:41984
	v_mfma_f32_32x32x16_bf16 v[18:33], v[138:141], v[94:97], v[18:33]
	ds_read_b128 v[114:117], v176 offset:43008
	ds_read_b128 v[118:121], v176 offset:44032
	ds_read_b128 v[122:125], v189 offset:58112
	ds_read_b128 v[126:129], v189 offset:58128
	ds_read_b128 v[130:133], v176 offset:45056
	ds_read_b128 v[134:137], v176 offset:46080
	ds_read_b128 v[138:141], v176 offset:47104
	ds_read_b128 v[142:145], v176 offset:48128
	ds_read_b128 v[190:193], v189 offset:58176
	ds_read_b128 v[194:197], v189 offset:58192
	v_mfma_f32_32x32x16_bf16 v[2:17], v[166:169], v[94:97], v[2:17]
	v_lshlrev_b32_e32 v152, 16, v110
	v_and_b32_e32 v153, 0xffff0000, v110
	v_lshlrev_b32_e32 v158, 16, v111
	v_and_b32_e32 v159, 0xffff0000, v111
	v_lshlrev_b32_e32 v110, 16, v112
	v_and_b32_e32 v111, 0xffff0000, v112
	v_lshlrev_b32_e32 v112, 16, v113
	v_and_b32_e32 v113, 0xffff0000, v113
	s_waitcnt lgkmcnt(0)
	v_pk_mul_f32 v[166:167], v[122:123], v[152:153]
	v_pk_mul_f32 v[168:169], v[124:125], v[158:159]
	v_pk_mul_f32 v[128:129], v[128:129], v[112:113]
	v_pk_mul_f32 v[126:127], v[126:127], v[110:111]
	v_cvt_pk_bf16_f32 v113, v128, v129
	v_cvt_pk_bf16_f32 v112, v126, v127
	v_cvt_pk_bf16_f32 v111, v168, v169
	v_cvt_pk_bf16_f32 v110, v166, v167
	v_pk_fma_f32 v[152:153], v[122:123], v[152:153], v[126:127]
	v_pk_fma_f32 v[158:159], v[124:125], v[158:159], v[128:129]
	v_mfma_f32_32x32x16_bf16 v[50:65], v[102:105], v[110:113], v[50:65]
	v_mfma_f32_32x32x16_bf16 v[34:49], v[106:109], v[110:113], v[34:49]
	v_mfma_f32_32x32x16_bf16 v[18:33], v[114:117], v[110:113], v[18:33]
	ds_read_b128 v[102:105], v176 offset:49152
	ds_read_b128 v[106:109], v176 offset:50176
	ds_read_b128 v[114:117], v176 offset:51200
	ds_read_b128 v[122:125], v176 offset:52224
	ds_read_b128 v[126:129], v189 offset:58240
	ds_read_b128 v[166:169], v189 offset:58256
	v_mfma_f32_32x32x16_bf16 v[2:17], v[118:121], v[110:113], v[2:17]
	v_lshlrev_b32_e32 v110, 16, v90
	v_and_b32_e32 v111, 0xffff0000, v90
	v_lshlrev_b32_e32 v112, 16, v91
	v_and_b32_e32 v113, 0xffff0000, v91
	v_lshlrev_b32_e32 v90, 16, v92
	v_and_b32_e32 v91, 0xffff0000, v92
	v_lshlrev_b32_e32 v92, 16, v93
	v_and_b32_e32 v93, 0xffff0000, v93
	v_pk_mul_f32 v[172:173], v[196:197], v[92:93]
	v_pk_mul_f32 v[184:185], v[194:195], v[90:91]
	v_pk_mul_f32 v[118:119], v[190:191], v[110:111]
	v_pk_mul_f32 v[120:121], v[192:193], v[112:113]
	v_pk_fma_f32 v[110:111], v[190:191], v[110:111], v[184:185]
	v_pk_fma_f32 v[112:113], v[192:193], v[112:113], v[172:173]
	v_pk_add_f32 v[110:111], v[152:153], v[110:111]
	v_pk_add_f32 v[112:113], v[158:159], v[112:113]
	v_cvt_pk_bf16_f32 v90, v118, v119
	v_pk_mov_b32 v[118:119], v[110:111], v[112:113] op_sel:[1,0]
	v_mov_b32_e32 v111, v113
	v_cvt_pk_bf16_f32 v93, v172, v173
	v_cvt_pk_bf16_f32 v92, v184, v185
	v_cvt_pk_bf16_f32 v91, v120, v121
	v_pk_add_f32 v[110:111], v[118:119], v[110:111]
	s_nop 0
	v_mfma_f32_32x32x16_bf16 v[50:65], v[130:133], v[90:93], v[50:65]
	v_add_f32_e64 v152, v110, v111
	v_add_f32_e64 v153, v111, v110
	v_mfma_f32_32x32x16_bf16 v[34:49], v[134:137], v[90:93], v[34:49]
	v_mfma_f32_32x32x16_bf16 v[18:33], v[138:141], v[90:93], v[18:33]
	ds_read_b128 v[110:113], v176 offset:53248
	ds_read_b128 v[118:121], v176 offset:54272
	ds_read_b128 v[130:133], v176 offset:55296
	ds_read_b128 v[134:137], v176 offset:56320
	ds_read_b128 v[138:141], v189 offset:58304
	ds_read_b128 v[190:193], v189 offset:58320
	v_mfma_f32_32x32x16_bf16 v[2:17], v[142:145], v[90:93], v[2:17]
	v_lshlrev_b32_e32 v90, 16, v86
	v_and_b32_e32 v91, 0xffff0000, v86
	v_lshlrev_b32_e32 v92, 16, v87
	v_and_b32_e32 v93, 0xffff0000, v87
	v_lshlrev_b32_e32 v86, 16, v88
	v_and_b32_e32 v87, 0xffff0000, v88
	v_lshlrev_b32_e32 v88, 16, v89
	v_and_b32_e32 v89, 0xffff0000, v89
	s_waitcnt lgkmcnt(0)
	v_pk_mul_f32 v[142:143], v[128:129], v[92:93]
	v_pk_mul_f32 v[144:145], v[126:127], v[90:91]
	v_pk_mul_f32 v[158:159], v[166:167], v[86:87]
	v_pk_mul_f32 v[166:167], v[168:169], v[88:89]
	v_cvt_pk_bf16_f32 v88, v158, v159
	v_cvt_pk_bf16_f32 v86, v144, v145
	v_cvt_pk_bf16_f32 v89, v166, v167
	v_cvt_pk_bf16_f32 v87, v142, v143
	v_pk_fma_f32 v[92:93], v[128:129], v[92:93], v[166:167]
	v_pk_fma_f32 v[90:91], v[126:127], v[90:91], v[158:159]
	v_mfma_f32_32x32x16_bf16 v[50:65], v[102:105], v[86:89], v[50:65]
	v_mfma_f32_32x32x16_bf16 v[34:49], v[106:109], v[86:89], v[34:49]
	v_mfma_f32_32x32x16_bf16 v[18:33], v[114:117], v[86:89], v[18:33]
	v_mfma_f32_32x32x16_bf16 v[2:17], v[122:125], v[86:89], v[2:17]
	v_lshlrev_b32_e32 v86, 16, v82
	v_and_b32_e32 v87, 0xffff0000, v82
	v_lshlrev_b32_e32 v88, 16, v83
	v_and_b32_e32 v89, 0xffff0000, v83
	v_lshlrev_b32_e32 v82, 16, v84
	v_and_b32_e32 v83, 0xffff0000, v84
	v_lshlrev_b32_e32 v84, 16, v85
	v_and_b32_e32 v85, 0xffff0000, v85
	v_mfma_f32_32x32x16_bf16 v[66:81], v[98:101], v[94:97], v[66:81]
	v_mul_f32_e64 v102, v140, v88
	v_mul_f32_e64 v103, v141, v89
	v_mul_f32_e64 v104, v138, v86
	v_mul_f32_e64 v105, v139, v87
	v_mul_f32_e64 v106, v190, v82
	v_mul_f32_e64 v107, v191, v83
	v_pk_mul_f32 v[108:109], v[192:193], v[84:85]
	v_cvt_pk_bf16_f32 v84, v106, v107
	v_cvt_pk_bf16_f32 v82, v104, v105
	v_cvt_pk_bf16_f32 v85, v108, v109
	v_cvt_pk_bf16_f32 v83, v102, v103
	s_waitcnt vmcnt(4) lgkmcnt(0)
	s_nop 0
	v_mfma_f32_32x32x16_bf16 v[50:65], v[110:113], v[82:85], v[50:65]
	s_barrier
	v_permlane32_swap_b32_e32 v162, v150
	v_permlane32_swap_b32_e32 v170, v148
	v_mov_b32_e32 v171, v162
	v_mov_b32_e32 v149, v150
	v_mfma_f32_32x32x16_bf16 v[34:49], v[118:121], v[82:85], v[34:49]
	v_add_f32_e64 v70, v170, v148
	v_add_f32_e64 v71, v171, v149
	s_mov_b32 s8, 0x3e3504f3
	v_add_f32_e64 v66, v66, v70
	v_add_f32_e64 v67, v67, v71
	v_or_b32_e32 v182, v182, v188
	v_mul_f32_e32 v74, v51, v51
	v_fmac_f32_e32 v74, v50, v50
	v_fmac_f32_e32 v74, v52, v52
	v_mfma_f32_32x32x16_bf16 v[18:33], v[130:133], v[82:85], v[18:33]
	v_fmac_f32_e32 v74, v53, v53
	v_fmac_f32_e32 v74, v54, v54
	v_fmac_f32_e32 v74, v55, v55
	v_fmac_f32_e32 v74, v56, v56
	v_fmac_f32_e32 v74, v57, v57
	v_fmac_f32_e32 v74, v58, v58
	v_fmac_f32_e32 v74, v59, v59
	v_mfma_f32_32x32x16_bf16 v[2:17], v[134:137], v[82:85], v[2:17]
	ds_read_b128 v[82:85], v147 offset:59904
	v_fmac_f32_e32 v74, v60, v60
	v_fmac_f32_e32 v74, v61, v61
	v_fmac_f32_e32 v74, v62, v62
	v_fmac_f32_e32 v74, v63, v63
	s_waitcnt lgkmcnt(0)
	v_pk_add_f32 v[66:67], v[82:83], v[66:67]
	v_fmac_f32_e32 v74, v64, v64
	v_pk_mul_f32 v[130:131], v[66:67], s[8:9] op_sel_hi:[1,0]
	v_lshlrev_b64 v[66:67], 5, v[182:183]
	v_lshl_add_u64 v[134:135], s[4:5], 0, v[66:67]
	v_add_f32_e32 v66, 0, v50
	v_add_f32_e32 v66, v66, v51
	v_add_f32_e32 v66, v66, v52
	v_add_f32_e32 v66, v66, v53
	v_add_f32_e32 v66, v66, v54
	v_add_f32_e32 v66, v66, v55
	v_add_f32_e32 v66, v66, v56
	v_add_f32_e32 v66, v66, v57
	v_add_f32_e32 v66, v66, v58
	v_add_f32_e32 v66, v66, v59
	v_add_f32_e32 v66, v66, v60
	v_add_f32_e32 v66, v66, v61
	v_add_f32_e32 v66, v66, v62
	v_add_f32_e32 v66, v66, v63
	v_add_f32_e32 v66, v66, v64
	v_add_f32_e32 v66, v66, v65
	v_fmac_f32_e32 v74, v65, v65
	v_add_f32_e32 v66, v66, v34
	v_fmac_f32_e32 v74, v34, v34
	v_add_f32_e32 v66, v66, v35
	v_fmac_f32_e32 v74, v35, v35
	v_add_f32_e32 v66, v66, v36
	v_fmac_f32_e32 v74, v36, v36
	v_add_f32_e32 v66, v66, v37
	v_fmac_f32_e32 v74, v37, v37
	v_add_f32_e32 v66, v66, v38
	v_fmac_f32_e32 v74, v38, v38
	v_add_f32_e32 v66, v66, v39
	v_fmac_f32_e32 v74, v39, v39
	v_add_f32_e32 v66, v66, v40
	v_fmac_f32_e32 v74, v40, v40
	v_add_f32_e32 v66, v66, v41
	v_fmac_f32_e32 v74, v41, v41
	v_add_f32_e32 v66, v66, v42
	v_fmac_f32_e32 v74, v42, v42
	v_add_f32_e32 v66, v66, v43
	v_fmac_f32_e32 v74, v43, v43
	v_add_f32_e32 v66, v66, v44
	v_fmac_f32_e32 v74, v44, v44
	v_add_f32_e32 v66, v66, v45
	v_fmac_f32_e32 v74, v45, v45
	v_add_f32_e32 v66, v66, v46
	v_fmac_f32_e32 v74, v46, v46
	v_add_f32_e32 v66, v66, v47
	v_fmac_f32_e32 v74, v47, v47
	v_add_f32_e32 v66, v66, v48
	v_fmac_f32_e32 v74, v48, v48
	v_add_f32_e32 v66, v66, v49
	v_fmac_f32_e32 v74, v49, v49
	v_add_f32_e32 v66, v66, v18
	v_fmac_f32_e32 v74, v18, v18
	v_add_f32_e32 v66, v66, v19
	v_fmac_f32_e32 v74, v19, v19
	v_add_f32_e32 v66, v66, v20
	v_fmac_f32_e32 v74, v20, v20
	v_add_f32_e32 v66, v66, v21
	v_fmac_f32_e32 v74, v21, v21
	v_add_f32_e32 v66, v66, v22
	v_fmac_f32_e32 v74, v22, v22
	v_add_f32_e32 v66, v66, v23
	v_fmac_f32_e32 v74, v23, v23
	v_add_f32_e32 v66, v66, v24
	v_fmac_f32_e32 v74, v24, v24
	v_add_f32_e32 v66, v66, v25
	v_fmac_f32_e32 v74, v25, v25
	v_add_f32_e32 v66, v66, v26
	v_fmac_f32_e32 v74, v26, v26
	v_add_f32_e32 v66, v66, v27
	v_fmac_f32_e32 v74, v27, v27
	v_add_f32_e32 v66, v66, v28
	v_fmac_f32_e32 v74, v28, v28
	v_add_f32_e32 v66, v66, v29
	v_fmac_f32_e32 v74, v29, v29
	v_add_f32_e32 v66, v66, v30
	v_fmac_f32_e32 v74, v30, v30
	v_add_f32_e32 v66, v66, v31
	v_fmac_f32_e32 v74, v31, v31
	v_add_f32_e32 v66, v66, v32
	v_fmac_f32_e32 v74, v32, v32
	v_add_f32_e32 v66, v66, v33
	v_fmac_f32_e32 v74, v33, v33
	v_add_f32_e32 v66, v66, v2
	v_fmac_f32_e32 v74, v2, v2
	v_pk_fma_f32 v[88:89], v[140:141], v[88:89], v[108:109]
	v_pk_fma_f32 v[86:87], v[138:139], v[86:87], v[106:107]
	v_add_f32_e32 v66, v66, v3
	v_fmac_f32_e32 v74, v3, v3
	v_pk_add_f32 v[86:87], v[90:91], v[86:87]
	v_pk_add_f32 v[88:89], v[92:93], v[88:89]
	v_add_f32_e32 v66, v66, v4
	v_fmac_f32_e32 v74, v4, v4
	v_pk_mov_b32 v[90:91], v[86:87], v[88:89] op_sel:[1,0]
	v_mov_b32_e32 v87, v89
	v_add_f32_e32 v66, v66, v5
	v_fmac_f32_e32 v74, v5, v5
	v_pk_add_f32 v[86:87], v[90:91], v[86:87]
	v_add_f32_e32 v66, v66, v6
	v_fmac_f32_e32 v74, v6, v6
	v_pk_add_f32 v[86:87], v[86:87], v[86:87] op_sel:[0,1] op_sel_hi:[1,0]
	v_add_f32_e32 v66, v66, v7
	v_fmac_f32_e32 v74, v7, v7
	v_permlane32_swap_b32_e32 v146, v86
	v_add_f32_e32 v66, v66, v8
	v_fmac_f32_e32 v74, v8, v8
	v_permlane32_swap_b32_e32 v156, v152
	v_mov_b32_e32 v157, v146
	v_mov_b32_e32 v153, v86
	v_add_f32_e32 v66, v66, v9
	v_fmac_f32_e32 v74, v9, v9
	v_pk_mul_f32 v[72:73], v[10:11], v[10:11]
	v_pk_add_f32 v[70:71], v[156:157], v[152:153]
	v_add_f32_e32 v66, v66, v10
	v_add_f32_e32 v72, v74, v72
	v_pk_add_f32 v[68:69], v[68:69], v[70:71]
	v_add_f32_e32 v75, v66, v11
	v_pk_mul_f32 v[70:71], v[12:13], v[12:13]
	v_add_f32_e32 v72, v72, v73
	v_pk_add_f32 v[68:69], v[84:85], v[68:69]
	v_add_f32_e32 v73, v75, v12
	v_add_f32_e32 v70, v72, v70
	v_pk_mul_f32 v[132:133], v[68:69], s[8:9] op_sel_hi:[1,0]
	v_pk_mul_f32 v[68:69], v[14:15], v[14:15]
	v_add_f32_e32 v73, v73, v13
	v_add_f32_e32 v70, v70, v71
	v_add_f32_e32 v71, v73, v14
	v_add_f32_e32 v68, v70, v68
	v_pk_mul_f32 v[66:67], v[16:17], v[16:17]
	v_add_f32_e32 v71, v71, v15
	v_add_f32_e32 v68, v68, v69
	v_add_f32_e32 v69, v71, v16
	v_add_f32_e32 v66, v68, v66
	v_add_f32_e32 v69, v69, v17
	v_add_f32_e32 v68, v66, v67
	v_mov_b32_e32 v67, v69
	v_mov_b32_e32 v66, v68
	s_nop 0
	v_permlane32_swap_b32_e32 v69, v67
	v_permlane32_swap_b32_e32 v68, v66
	v_pk_add_f32 v[66:67], v[68:69], v[66:67]
	v_mov_b32_e32 v155, v175
	v_pk_mul_f32 v[136:137], v[66:67], s[0:1] op_sel_hi:[1,0]
	v_readfirstlane_b32 s0, v187
	v_fma_f32 v66, -v137, v137, v136
	v_add_f32_e32 v66, 0x3727c5ac, v66
	v_cmp_gt_f32_e32 vcc, s2, v66
	s_mov_b64 s[2:3], 0x22000
	v_mul_f32_e32 v67, 0x4b800000, v66
	v_lshl_add_u64 v[138:139], v[180:181], 0, s[2:3]
	s_mov_b32 m0, s0
	v_cndmask_b32_e32 v136, v66, v67, vcc
	ds_read_b128 v[114:117], v147 offset:58880
	ds_read_b128 v[118:121], v147 offset:58912
	ds_read_b128 v[122:125], v147 offset:58944
	ds_read_b128 v[126:129], v147 offset:58976
	ds_read_b128 v[98:101], v147 offset:59008
	ds_read_b128 v[102:105], v147 offset:59040
	ds_read_b128 v[106:109], v147 offset:59072
	ds_read_b128 v[110:113], v147 offset:59104
	ds_read_b128 v[82:85], v147 offset:59136
	ds_read_b128 v[86:89], v147 offset:59168
	ds_read_b128 v[90:93], v147 offset:59200
	ds_read_b128 v[94:97], v147 offset:59232
	ds_read_b128 v[66:69], v147 offset:59264
	ds_read_b128 v[70:73], v147 offset:59296
	ds_read_b128 v[74:77], v147 offset:59328
	ds_read_b128 v[78:81], v147 offset:59360
	global_load_lds_dwordx4 v[138:139], off
	global_load_lds_dwordx4 v[138:139], off offset:1024
	global_load_lds_dwordx4 v[138:139], off offset:2048
	global_load_lds_dwordx4 v[138:139], off offset:3072
	v_rsq_f32_e32 v136, v136
	v_lshl_add_u64 v[134:135], v[134:135], 0, v[154:155]
	global_store_dwordx4 v[134:135], v[130:133], off nt
	s_nop 1
	v_mul_f32_e32 v130, 0x45800000, v136
	v_cndmask_b32_e32 v162, v136, v130, vcc
	v_mul_f32_e64 v166, v162, -v137
	v_pk_fma_f32 v[134:135], v[162:163], v[50:51], v[166:167] op_sel_hi:[0,1,0]
	v_pk_fma_f32 v[130:131], v[162:163], v[52:53], v[166:167] op_sel_hi:[0,1,0]
	v_pk_fma_f32 v[136:137], v[162:163], v[54:55], v[166:167] op_sel_hi:[0,1,0]
	v_pk_fma_f32 v[132:133], v[162:163], v[56:57], v[166:167] op_sel_hi:[0,1,0]
	v_cvt_pk_bf16_f32 v133, v132, v133
	v_cvt_pk_bf16_f32 v132, v136, v137
	v_cvt_pk_bf16_f32 v131, v130, v131
	v_cvt_pk_bf16_f32 v130, v134, v135
	v_pk_fma_f32 v[138:139], v[162:163], v[58:59], v[166:167] op_sel_hi:[0,1,0]
	v_pk_fma_f32 v[134:135], v[162:163], v[60:61], v[166:167] op_sel_hi:[0,1,0]
	v_pk_fma_f32 v[140:141], v[162:163], v[62:63], v[166:167] op_sel_hi:[0,1,0]
	v_pk_fma_f32 v[136:137], v[162:163], v[64:65], v[166:167] op_sel_hi:[0,1,0]
	v_cvt_pk_bf16_f32 v137, v136, v137
	v_cvt_pk_bf16_f32 v136, v140, v141
	v_cvt_pk_bf16_f32 v135, v134, v135
	v_cvt_pk_bf16_f32 v134, v138, v139
	v_pk_fma_f32 v[142:143], v[162:163], v[34:35], v[166:167] op_sel_hi:[0,1,0]
	v_pk_fma_f32 v[138:139], v[162:163], v[36:37], v[166:167] op_sel_hi:[0,1,0]
	v_pk_fma_f32 v[144:145], v[162:163], v[38:39], v[166:167] op_sel_hi:[0,1,0]
	v_pk_fma_f32 v[140:141], v[162:163], v[40:41], v[166:167] op_sel_hi:[0,1,0]
	v_cvt_pk_bf16_f32 v141, v140, v141
	v_cvt_pk_bf16_f32 v140, v144, v145
	v_cvt_pk_bf16_f32 v139, v138, v139
	v_cvt_pk_bf16_f32 v138, v142, v143
	v_pk_fma_f32 v[146:147], v[162:163], v[42:43], v[166:167] op_sel_hi:[0,1,0]
	v_pk_fma_f32 v[142:143], v[162:163], v[44:45], v[166:167] op_sel_hi:[0,1,0]
	v_pk_fma_f32 v[148:149], v[162:163], v[46:47], v[166:167] op_sel_hi:[0,1,0]
	v_pk_fma_f32 v[144:145], v[162:163], v[48:49], v[166:167] op_sel_hi:[0,1,0]
	v_cvt_pk_bf16_f32 v145, v144, v145
	v_cvt_pk_bf16_f32 v144, v148, v149
	v_cvt_pk_bf16_f32 v143, v142, v143
	v_cvt_pk_bf16_f32 v142, v146, v147
	v_pk_fma_f32 v[150:151], v[162:163], v[18:19], v[166:167] op_sel_hi:[0,1,0]
	v_pk_fma_f32 v[146:147], v[162:163], v[20:21], v[166:167] op_sel_hi:[0,1,0]
	v_pk_fma_f32 v[152:153], v[162:163], v[22:23], v[166:167] op_sel_hi:[0,1,0]
	v_pk_fma_f32 v[148:149], v[162:163], v[24:25], v[166:167] op_sel_hi:[0,1,0]
	v_cvt_pk_bf16_f32 v149, v148, v149
	v_cvt_pk_bf16_f32 v148, v152, v153
	v_cvt_pk_bf16_f32 v147, v146, v147
	v_cvt_pk_bf16_f32 v146, v150, v151
	v_pk_fma_f32 v[156:157], v[162:163], v[26:27], v[166:167] op_sel_hi:[0,1,0]
	v_pk_fma_f32 v[150:151], v[162:163], v[28:29], v[166:167] op_sel_hi:[0,1,0]
	v_pk_fma_f32 v[158:159], v[162:163], v[30:31], v[166:167] op_sel_hi:[0,1,0]
	v_pk_fma_f32 v[152:153], v[162:163], v[32:33], v[166:167] op_sel_hi:[0,1,0]
	v_cvt_pk_bf16_f32 v153, v152, v153
	v_cvt_pk_bf16_f32 v152, v158, v159
	v_cvt_pk_bf16_f32 v151, v150, v151
	v_cvt_pk_bf16_f32 v150, v156, v157
	v_pk_fma_f32 v[168:169], v[162:163], v[2:3], v[166:167] op_sel_hi:[0,1,0]
	v_pk_fma_f32 v[156:157], v[162:163], v[4:5], v[166:167] op_sel_hi:[0,1,0]
	v_pk_fma_f32 v[170:171], v[162:163], v[6:7], v[166:167] op_sel_hi:[0,1,0]
	v_pk_fma_f32 v[158:159], v[162:163], v[8:9], v[166:167] op_sel_hi:[0,1,0]
	v_cvt_pk_bf16_f32 v159, v158, v159
	v_cvt_pk_bf16_f32 v158, v170, v171
	v_cvt_pk_bf16_f32 v157, v156, v157
	v_cvt_pk_bf16_f32 v156, v168, v169
	v_pk_fma_f32 v[212:213], v[162:163], v[10:11], v[166:167] op_sel_hi:[0,1,0]
	v_pk_fma_f32 v[208:209], v[162:163], v[12:13], v[166:167] op_sel_hi:[0,1,0]
	v_pk_fma_f32 v[214:215], v[162:163], v[14:15], v[166:167] op_sel_hi:[0,1,0]
	v_pk_fma_f32 v[210:211], v[162:163], v[16:17], v[166:167] op_sel_hi:[0,1,0]
	ds_read_b128 v[166:169], v176
	ds_read_b128 v[170:173], v176 offset:1024
	ds_read_b128 v[182:185], v176 offset:2048
	ds_read_b128 v[188:191], v176 offset:3072
	ds_read_b128 v[192:195], v176 offset:4096
	ds_read_b128 v[196:199], v176 offset:5120
	ds_read_b128 v[200:203], v176 offset:6144
	ds_read_b128 v[204:207], v176 offset:7168
	v_cvt_pk_bf16_f32 v211, v210, v211
	v_cvt_pk_bf16_f32 v210, v214, v215
	v_cvt_pk_bf16_f32 v209, v208, v209
	v_cvt_pk_bf16_f32 v208, v212, v213
	s_waitcnt lgkmcnt(0)
	v_mfma_f32_32x32x16_bf16 v[114:129], v[166:169], v[130:133], v[114:129]
	v_mfma_f32_32x32x16_bf16 v[98:113], v[170:173], v[130:133], v[98:113]
	v_mfma_f32_32x32x16_bf16 v[82:97], v[182:185], v[130:133], v[82:97]
	ds_read_b128 v[166:169], v176 offset:8192
	ds_read_b128 v[170:173], v176 offset:9216
	ds_read_b128 v[182:185], v176 offset:10240
	ds_read_b128 v[212:215], v176 offset:11264
	v_mfma_f32_32x32x16_bf16 v[66:81], v[188:191], v[130:133], v[66:81]
	v_mfma_f32_32x32x16_bf16 v[114:129], v[192:195], v[134:137], v[114:129]
	v_mfma_f32_32x32x16_bf16 v[98:113], v[196:199], v[134:137], v[98:113]
	ds_read_b128 v[130:133], v176 offset:12288
	ds_read_b128 v[188:191], v176 offset:13312
	ds_read_b128 v[192:195], v176 offset:14336
	ds_read_b128 v[196:199], v176 offset:15360
	v_mfma_f32_32x32x16_bf16 v[82:97], v[200:203], v[134:137], v[82:97]
	v_mfma_f32_32x32x16_bf16 v[66:81], v[204:207], v[134:137], v[66:81]
	s_waitcnt lgkmcnt(0)
	v_mfma_f32_32x32x16_bf16 v[114:129], v[166:169], v[138:141], v[114:129]
	v_mfma_f32_32x32x16_bf16 v[98:113], v[170:173], v[138:141], v[98:113]
	v_mfma_f32_32x32x16_bf16 v[82:97], v[182:185], v[138:141], v[82:97]
	v_mfma_f32_32x32x16_bf16 v[66:81], v[212:215], v[138:141], v[66:81]
	s_mov_b64 s[2:3], 0x26000
	v_readfirstlane_b32 s0, v186
	v_mfma_f32_32x32x16_bf16 v[114:129], v[130:133], v[142:145], v[114:129]
	v_lshl_add_u64 v[130:131], v[180:181], 0, s[2:3]
	s_mov_b32 m0, s0
	s_waitcnt vmcnt(4) lgkmcnt(0)
	s_barrier
	global_load_lds_dwordx4 v[130:131], off
	global_load_lds_dwordx4 v[130:131], off offset:1024
	global_load_lds_dwordx4 v[130:131], off offset:2048
	global_load_lds_dwordx4 v[130:131], off offset:3072
	v_mfma_f32_32x32x16_bf16 v[98:113], v[188:191], v[142:145], v[98:113]
	ds_read_b128 v[130:133], v176 offset:20480
	ds_read_b128 v[134:137], v176 offset:21504
	ds_read_b128 v[138:141], v176 offset:22528
	ds_read_b128 v[166:169], v176 offset:23552
	ds_read_b128 v[170:173], v176 offset:24576
	ds_read_b128 v[180:183], v176 offset:25600
	ds_read_b128 v[184:187], v176 offset:26624
	ds_read_b128 v[188:191], v176 offset:27648
	v_mfma_f32_32x32x16_bf16 v[82:97], v[192:195], v[142:145], v[82:97]
	v_mfma_f32_32x32x16_bf16 v[66:81], v[196:199], v[142:145], v[66:81]
	s_waitcnt lgkmcnt(0)
	v_mfma_f32_32x32x16_bf16 v[114:129], v[130:133], v[146:149], v[114:129]
	v_mfma_f32_32x32x16_bf16 v[98:113], v[134:137], v[146:149], v[98:113]
	v_mfma_f32_32x32x16_bf16 v[82:97], v[138:141], v[146:149], v[82:97]
	ds_read_b128 v[130:133], v176 offset:28672
	ds_read_b128 v[134:137], v176 offset:29696
	ds_read_b128 v[138:141], v176 offset:30720
	ds_read_b128 v[142:145], v176 offset:31744
	v_mfma_f32_32x32x16_bf16 v[66:81], v[166:169], v[146:149], v[66:81]
	v_mfma_f32_32x32x16_bf16 v[114:129], v[170:173], v[150:153], v[114:129]
	v_mfma_f32_32x32x16_bf16 v[98:113], v[180:183], v[150:153], v[98:113]
	ds_read_b128 v[146:149], v176 offset:32768
	ds_read_b128 v[166:169], v176 offset:33792
	ds_read_b128 v[170:173], v176 offset:34816
	ds_read_b128 v[180:183], v176 offset:35840
	v_mfma_f32_32x32x16_bf16 v[82:97], v[184:187], v[150:153], v[82:97]
	v_mfma_f32_32x32x16_bf16 v[66:81], v[188:191], v[150:153], v[66:81]
	s_waitcnt lgkmcnt(0)
	v_mfma_f32_32x32x16_bf16 v[114:129], v[130:133], v[156:159], v[114:129]
	v_mfma_f32_32x32x16_bf16 v[98:113], v[134:137], v[156:159], v[98:113]
	v_mfma_f32_32x32x16_bf16 v[82:97], v[138:141], v[156:159], v[82:97]
	v_mfma_f32_32x32x16_bf16 v[66:81], v[142:145], v[156:159], v[66:81]
	v_mfma_f32_32x32x16_bf16 v[114:129], v[146:149], v[208:211], v[114:129]
	s_waitcnt vmcnt(4) lgkmcnt(0)
	s_barrier
	v_mfma_f32_32x32x16_bf16 v[98:113], v[166:169], v[208:211], v[98:113]
	s_nop 8
	v_mul_f32_e32 v130, 0x3c23d70a, v114
	v_mul_f32_e32 v131, 0x3c23d70a, v115
	v_max_f32_e32 v114, v114, v130
	v_mul_f32_e32 v130, 0x3c23d70a, v116
	v_max_f32_e32 v115, v115, v131
	v_max_f32_e32 v116, v116, v130
	v_mul_f32_e32 v130, 0x3c23d70a, v117
	v_max_f32_e32 v117, v117, v130
	v_cvt_pk_bf16_f32 v134, v114, v115
	v_mul_f32_e32 v114, 0x3c23d70a, v122
	v_cvt_pk_bf16_f32 v135, v116, v117
	v_max_f32_e32 v114, v122, v114
	v_mul_f32_e32 v115, 0x3c23d70a, v123
	v_mfma_f32_32x32x16_bf16 v[82:97], v[170:173], v[208:211], v[82:97]
	v_max_f32_e32 v115, v123, v115
	v_cvt_pk_bf16_f32 v138, v114, v115
	v_mul_f32_e32 v114, 0x3c23d70a, v98
	v_max_f32_e32 v98, v98, v114
	v_mul_f32_e32 v114, 0x3c23d70a, v99
	v_max_f32_e32 v99, v99, v114
	v_mul_f32_e32 v114, 0x3c23d70a, v100
	v_max_f32_e32 v100, v100, v114
	v_mul_f32_e32 v114, 0x3c23d70a, v101
	v_max_f32_e32 v101, v101, v114
	v_cvt_pk_bf16_f32 v142, v98, v99
	v_mul_f32_e32 v98, 0x3c23d70a, v106
	v_cvt_pk_bf16_f32 v143, v100, v101
	v_max_f32_e32 v98, v106, v98
	v_mul_f32_e32 v99, 0x3c23d70a, v107
	v_mfma_f32_32x32x16_bf16 v[66:81], v[180:183], v[208:211], v[66:81]
	v_max_f32_e32 v99, v107, v99
	v_cvt_pk_bf16_f32 v146, v98, v99
	v_mul_f32_e32 v98, 0x3c23d70a, v82
	v_max_f32_e32 v82, v82, v98
	v_mul_f32_e32 v98, 0x3c23d70a, v83
	v_max_f32_e32 v83, v83, v98
	v_mul_f32_e32 v98, 0x3c23d70a, v84
	v_max_f32_e32 v84, v84, v98
	v_mul_f32_e32 v98, 0x3c23d70a, v85
	v_max_f32_e32 v85, v85, v98
	v_cvt_pk_bf16_f32 v150, v82, v83
	v_mul_f32_e32 v82, 0x3c23d70a, v90
	v_cvt_pk_bf16_f32 v151, v84, v85
	v_max_f32_e32 v82, v90, v82
	v_mul_f32_e32 v83, 0x3c23d70a, v91
	v_max_f32_e32 v83, v91, v83
	v_mul_f32_e32 v130, 0x3c23d70a, v118
	v_cvt_pk_bf16_f32 v156, v82, v83
	v_mul_f32_e32 v82, 0x3c23d70a, v66
	v_max_f32_e32 v118, v118, v130
	v_mul_f32_e32 v130, 0x3c23d70a, v119
	v_max_f32_e32 v66, v66, v82
	v_mul_f32_e32 v82, 0x3c23d70a, v67
	v_max_f32_e32 v119, v119, v130
	v_mul_f32_e32 v130, 0x3c23d70a, v120
	v_mul_f32_e32 v114, 0x3c23d70a, v102
	v_mul_f32_e32 v98, 0x3c23d70a, v86
	v_max_f32_e32 v67, v67, v82
	v_max_f32_e32 v120, v120, v130
	v_mul_f32_e32 v130, 0x3c23d70a, v121
	v_max_f32_e32 v102, v102, v114
	v_mul_f32_e32 v114, 0x3c23d70a, v103
	v_max_f32_e32 v86, v86, v98
	v_mul_f32_e32 v98, 0x3c23d70a, v87
	v_cvt_pk_bf16_f32 v166, v66, v67
	v_mul_f32_e32 v66, 0x3c23d70a, v74
	v_max_f32_e32 v121, v121, v130
	v_mul_f32_e32 v116, 0x3c23d70a, v124
	v_max_f32_e32 v103, v103, v114
	v_mul_f32_e32 v114, 0x3c23d70a, v104
	v_mul_f32_e32 v100, 0x3c23d70a, v108
	v_max_f32_e32 v87, v87, v98
	v_mul_f32_e32 v98, 0x3c23d70a, v88
	v_mul_f32_e32 v84, 0x3c23d70a, v92
	v_mul_f32_e32 v82, 0x3c23d70a, v68
	v_max_f32_e32 v130, v74, v66
	v_mul_f32_e32 v66, 0x3c23d70a, v75
	v_cvt_pk_bf16_f32 v136, v118, v119
	v_max_f32_e32 v116, v124, v116
	v_mul_f32_e32 v117, 0x3c23d70a, v125
	v_max_f32_e32 v104, v104, v114
	v_mul_f32_e32 v114, 0x3c23d70a, v105
	v_cvt_pk_bf16_f32 v144, v102, v103
	v_max_f32_e32 v100, v108, v100
	v_mul_f32_e32 v101, 0x3c23d70a, v109
	v_max_f32_e32 v88, v88, v98
	v_mul_f32_e32 v98, 0x3c23d70a, v89
	v_cvt_pk_bf16_f32 v152, v86, v87
	v_max_f32_e32 v84, v92, v84
	v_mul_f32_e32 v85, 0x3c23d70a, v93
	v_max_f32_e32 v68, v68, v82
	v_mul_f32_e32 v82, 0x3c23d70a, v69
	v_max_f32_e32 v155, v75, v66
	v_mul_f32_e32 v66, 0x3c23d70a, v76
	v_max_f32_e32 v117, v125, v117
	v_mul_f32_e32 v118, 0x3c23d70a, v126
	v_max_f32_e32 v105, v105, v114
	v_max_f32_e32 v101, v109, v101
	v_mul_f32_e32 v102, 0x3c23d70a, v110
	v_max_f32_e32 v89, v89, v98
	v_max_f32_e32 v85, v93, v85
	v_mul_f32_e32 v86, 0x3c23d70a, v94
	v_max_f32_e32 v69, v69, v82
	v_mul_f32_e32 v82, 0x3c23d70a, v70
	v_max_f32_e32 v131, v76, v66
	v_mul_f32_e32 v66, 0x3c23d70a, v77
	v_cvt_pk_bf16_f32 v137, v120, v121
	v_max_f32_e32 v118, v126, v118
	v_mul_f32_e32 v119, 0x3c23d70a, v127
	v_cvt_pk_bf16_f32 v145, v104, v105
	v_max_f32_e32 v102, v110, v102
	v_mul_f32_e32 v103, 0x3c23d70a, v111
	v_cvt_pk_bf16_f32 v153, v88, v89
	v_max_f32_e32 v86, v94, v86
	v_mul_f32_e32 v87, 0x3c23d70a, v95
	v_max_f32_e32 v70, v70, v82
	v_mul_f32_e32 v82, 0x3c23d70a, v71
	v_max_f32_e32 v162, v77, v66
	v_mul_f32_e32 v66, 0x3c23d70a, v78
	v_max_f32_e32 v119, v127, v119
	v_mul_f32_e32 v120, 0x3c23d70a, v128
	v_max_f32_e32 v103, v111, v103
	v_mul_f32_e32 v104, 0x3c23d70a, v112
	v_max_f32_e32 v87, v95, v87
	v_mul_f32_e32 v88, 0x3c23d70a, v96
	v_max_f32_e32 v71, v71, v82
	v_mul_f32_e32 v82, 0x3c23d70a, v72
	v_max_f32_e32 v132, v78, v66
	v_mul_f32_e32 v66, 0x3c23d70a, v79
	v_max_f32_e32 v120, v128, v120
	v_mul_f32_e32 v121, 0x3c23d70a, v129
	v_max_f32_e32 v104, v112, v104
	v_mul_f32_e32 v105, 0x3c23d70a, v113
	v_max_f32_e32 v88, v96, v88
	v_mul_f32_e32 v89, 0x3c23d70a, v97
	v_max_f32_e32 v72, v72, v82
	v_mul_f32_e32 v82, 0x3c23d70a, v73
	v_max_f32_e32 v174, v79, v66
	v_mul_f32_e32 v66, 0x3c23d70a, v80
	v_max_f32_e32 v121, v129, v121
	v_max_f32_e32 v105, v113, v105
	v_max_f32_e32 v89, v97, v89
	v_max_f32_e32 v73, v73, v82
	v_max_f32_e32 v133, v80, v66
	v_mul_f32_e32 v66, 0x3c23d70a, v81
	v_cvt_pk_bf16_f32 v141, v120, v121
	v_cvt_pk_bf16_f32 v140, v118, v119
	v_cvt_pk_bf16_f32 v139, v116, v117
	v_cvt_pk_bf16_f32 v149, v104, v105
	v_cvt_pk_bf16_f32 v148, v102, v103
	v_cvt_pk_bf16_f32 v147, v100, v101
	v_cvt_pk_bf16_f32 v159, v88, v89
	v_cvt_pk_bf16_f32 v158, v86, v87
	v_cvt_pk_bf16_f32 v157, v84, v85
	v_cvt_pk_bf16_f32 v169, v72, v73
	v_cvt_pk_bf16_f32 v168, v70, v71
	v_cvt_pk_bf16_f32 v167, v68, v69
	v_max_f32_e32 v177, v81, v66
	ds_read_b128 v[114:117], v154 offset:59392
	ds_read_b128 v[118:121], v154 offset:59424
	ds_read_b128 v[122:125], v154 offset:59456
	ds_read_b128 v[126:129], v154 offset:59488
	ds_read_b128 v[98:101], v154 offset:59520
	ds_read_b128 v[102:105], v154 offset:59552
	ds_read_b128 v[106:109], v154 offset:59584
	ds_read_b128 v[110:113], v154 offset:59616
	ds_read_b128 v[82:85], v154 offset:59648
	ds_read_b128 v[86:89], v154 offset:59680
	ds_read_b128 v[90:93], v154 offset:59712
	ds_read_b128 v[94:97], v154 offset:59744
	ds_read_b128 v[66:69], v154 offset:59776
	ds_read_b128 v[70:73], v154 offset:59808
	ds_read_b128 v[74:77], v154 offset:59840
	ds_read_b128 v[78:81], v154 offset:59872
	ds_read_b128 v[170:173], v176 offset:40960
	ds_read_b128 v[180:183], v176 offset:41984
	ds_read_b128 v[184:187], v176 offset:43008
	ds_read_b128 v[188:191], v176 offset:44032
	ds_read_b128 v[192:195], v176 offset:45056
	ds_read_b128 v[196:199], v176 offset:46080
	ds_read_b128 v[200:203], v176 offset:47104
	ds_read_b128 v[204:207], v176 offset:48128
	v_cvt_pk_bf16_f32 v133, v133, v177
	v_cvt_pk_bf16_f32 v132, v132, v174
	v_cvt_pk_bf16_f32 v131, v131, v162
	v_cvt_pk_bf16_f32 v130, v130, v155
	s_waitcnt lgkmcnt(0)
	v_mfma_f32_32x32x16_bf16 v[114:129], v[170:173], v[134:137], v[114:129]
	v_mfma_f32_32x32x16_bf16 v[98:113], v[180:183], v[134:137], v[98:113]
	v_mfma_f32_32x32x16_bf16 v[82:97], v[184:187], v[134:137], v[82:97]
	ds_read_b128 v[170:173], v176 offset:49152
	ds_read_b128 v[180:183], v176 offset:50176
	ds_read_b128 v[184:187], v176 offset:51200
	ds_read_b128 v[208:211], v176 offset:52224
	v_mfma_f32_32x32x16_bf16 v[66:81], v[188:191], v[134:137], v[66:81]
	v_mfma_f32_32x32x16_bf16 v[114:129], v[192:195], v[138:141], v[114:129]
	v_mfma_f32_32x32x16_bf16 v[98:113], v[196:199], v[138:141], v[98:113]
	ds_read_b128 v[134:137], v176 offset:53248
	ds_read_b128 v[188:191], v176 offset:54272
	ds_read_b128 v[192:195], v176 offset:55296
	ds_read_b128 v[196:199], v176 offset:56320
	v_mfma_f32_32x32x16_bf16 v[82:97], v[200:203], v[138:141], v[82:97]
	v_mfma_f32_32x32x16_bf16 v[66:81], v[204:207], v[138:141], v[66:81]
	s_waitcnt lgkmcnt(0)
	v_mfma_f32_32x32x16_bf16 v[114:129], v[170:173], v[142:145], v[114:129]
	v_mfma_f32_32x32x16_bf16 v[98:113], v[180:183], v[142:145], v[98:113]
	v_mfma_f32_32x32x16_bf16 v[82:97], v[184:187], v[142:145], v[82:97]
	v_mfma_f32_32x32x16_bf16 v[66:81], v[208:211], v[142:145], v[66:81]
	v_mfma_f32_32x32x16_bf16 v[114:129], v[134:137], v[146:149], v[114:129]
	s_waitcnt vmcnt(0) lgkmcnt(0)
	s_barrier
	v_mfma_f32_32x32x16_bf16 v[98:113], v[188:191], v[146:149], v[98:113]
	v_mfma_f32_32x32x16_bf16 v[82:97], v[192:195], v[146:149], v[82:97]
	ds_read_b128 v[134:137], v176
	ds_read_b128 v[138:141], v176 offset:1024
	ds_read_b128 v[142:145], v176 offset:2048
	ds_read_b128 v[170:173], v176 offset:3072
	ds_read_b128 v[180:183], v176 offset:4096
	ds_read_b128 v[184:187], v176 offset:5120
	ds_read_b128 v[188:191], v176 offset:6144
	ds_read_b128 v[192:195], v176 offset:7168
	v_mfma_f32_32x32x16_bf16 v[66:81], v[196:199], v[146:149], v[66:81]
	s_waitcnt lgkmcnt(5)
	v_mfma_f32_32x32x16_bf16 v[82:97], v[142:145], v[150:153], v[82:97]
	ds_read_b128 v[142:145], v176 offset:8192
	ds_read_b128 v[146:149], v176 offset:9216
	ds_read_b128 v[196:199], v176 offset:10240
	ds_read_b128 v[200:203], v176 offset:11264
	v_mfma_f32_32x32x16_bf16 v[114:129], v[134:137], v[150:153], v[114:129]
	v_mfma_f32_32x32x16_bf16 v[98:113], v[138:141], v[150:153], v[98:113]
	s_waitcnt lgkmcnt(8)
	v_mfma_f32_32x32x16_bf16 v[66:81], v[170:173], v[150:153], v[66:81]
	ds_read_b128 v[150:153], v176 offset:12288
	ds_read_b128 v[170:173], v176 offset:13312
	ds_read_b128 v[138:141], v176 offset:14336
	ds_read_b128 v[134:137], v176 offset:15360
	s_waitcnt lgkmcnt(11)
	v_mfma_f32_32x32x16_bf16 v[114:129], v[180:183], v[156:159], v[114:129]
	s_waitcnt lgkmcnt(10)
	v_mfma_f32_32x32x16_bf16 v[98:113], v[184:187], v[156:159], v[98:113]
	s_waitcnt lgkmcnt(9)
	v_mfma_f32_32x32x16_bf16 v[82:97], v[188:191], v[156:159], v[82:97]
	s_waitcnt lgkmcnt(8)
	v_mfma_f32_32x32x16_bf16 v[66:81], v[192:195], v[156:159], v[66:81]
	s_waitcnt lgkmcnt(7)
	v_mfma_f32_32x32x16_bf16 v[114:129], v[142:145], v[166:169], v[114:129]
	s_waitcnt lgkmcnt(6)
	v_mfma_f32_32x32x16_bf16 v[98:113], v[146:149], v[166:169], v[98:113]
	s_waitcnt lgkmcnt(5)
	v_mfma_f32_32x32x16_bf16 v[82:97], v[196:199], v[166:169], v[82:97]
	s_waitcnt lgkmcnt(4)
	v_mfma_f32_32x32x16_bf16 v[66:81], v[200:203], v[166:169], v[66:81]
	s_waitcnt lgkmcnt(3)
	v_mfma_f32_32x32x16_bf16 v[114:129], v[150:153], v[130:133], v[114:129]
	v_and_b32_e32 v0, 7, v0
	v_lshlrev_b32_e32 v174, 4, v0
	v_or_b32_e32 v144, v1, v174
	v_mad_u32_u24 v145, v161, s1, v144
	v_lshl_add_u64 v[142:143], s[6:7], 0, v[178:179]
	s_nop 6
	v_mul_f32_e32 v0, 0x3c23d70a, v114
	v_max_f32_e32 v0, v114, v0
	v_mul_f32_e32 v1, 0x3c23d70a, v115
	v_max_f32_e32 v1, v115, v1
	v_pk_add_f32 v[50:51], v[50:51], v[0:1]
	v_mul_f32_e32 v0, 0x3c23d70a, v116
	v_max_f32_e32 v0, v116, v0
	v_mul_f32_e32 v1, 0x3c23d70a, v117
	v_max_f32_e32 v114, v117, v117
	v_max_f32_e32 v1, v114, v1
	v_pk_add_f32 v[52:53], v[52:53], v[0:1]
	v_mul_f32_e32 v0, 0x3c23d70a, v118
	ds_write_b128 v160, v[50:53] offset:61440
	v_max_f32_e32 v0, v118, v0
	v_mul_f32_e32 v1, 0x3c23d70a, v119
	v_max_f32_e32 v1, v119, v1
	v_pk_add_f32 v[50:51], v[54:55], v[0:1]
	v_mul_f32_e32 v0, 0x3c23d70a, v120
	v_max_f32_e32 v0, v120, v0
	v_mul_f32_e32 v1, 0x3c23d70a, v121
	v_max_f32_e32 v1, v121, v1
	v_pk_add_f32 v[52:53], v[56:57], v[0:1]
	v_mul_f32_e32 v0, 0x3c23d70a, v122
	ds_write_b128 v160, v[50:53] offset:61472
	v_max_f32_e32 v0, v122, v0
	v_mul_f32_e32 v1, 0x3c23d70a, v123
	v_max_f32_e32 v1, v123, v1
	v_pk_add_f32 v[50:51], v[58:59], v[0:1]
	v_mul_f32_e32 v0, 0x3c23d70a, v124
	v_max_f32_e32 v0, v124, v0
	v_mul_f32_e32 v1, 0x3c23d70a, v125
	v_max_f32_e32 v1, v125, v1
	v_pk_add_f32 v[52:53], v[60:61], v[0:1]
	v_mul_f32_e32 v0, 0x3c23d70a, v126
	ds_write_b128 v160, v[50:53] offset:61504
	v_max_f32_e32 v0, v126, v0
	v_mul_f32_e32 v1, 0x3c23d70a, v127
	v_max_f32_e32 v1, v127, v1
	v_pk_add_f32 v[50:51], v[62:63], v[0:1]
	v_mul_f32_e32 v0, 0x3c23d70a, v128
	v_max_f32_e32 v0, v128, v0
	v_mul_f32_e32 v1, 0x3c23d70a, v129
	v_max_f32_e32 v1, v129, v1
	v_pk_add_f32 v[52:53], v[64:65], v[0:1]
	ds_write_b128 v160, v[50:53] offset:61536
	ds_read_b128 v[50:53], v145 offset:61440
	v_add_u32_e32 v62, v144, v165
	ds_read_b128 v[54:57], v62 offset:61440
	v_lshl_add_u64 v[142:143], v[142:143], 0, v[174:175]
	v_lshlrev_b32_e32 v174, 9, v161
	s_waitcnt lgkmcnt(8)
	v_mfma_f32_32x32x16_bf16 v[98:113], v[170:173], v[130:133], v[98:113]
	v_lshl_add_u64 v[0:1], v[142:143], 0, v[174:175]
	s_waitcnt lgkmcnt(1)
	global_store_dwordx4 v[0:1], v[50:53], off nt
	v_add_u32_e32 v63, v144, v164
	v_add_u32_e32 v64, v144, v163
	v_or_b32_e32 v50, 0x1000, v174
	v_mov_b32_e32 v51, v175
	v_lshl_add_u64 v[50:51], v[142:143], 0, v[50:51]
	ds_read_b128 v[58:61], v64 offset:61440
	s_waitcnt lgkmcnt(1)
	global_store_dwordx4 v[50:51], v[54:57], off nt
	ds_read_b128 v[54:57], v63 offset:61440
	v_or_b32_e32 v52, 0x2000, v174
	v_mov_b32_e32 v53, v175
	v_lshl_add_u64 v[52:53], v[142:143], 0, v[52:53]
	v_or_b32_e32 v174, 0x3000, v174
	s_waitcnt lgkmcnt(0)
	global_store_dwordx4 v[52:53], v[54:57], off nt
	v_mfma_f32_32x32x16_bf16 v[82:97], v[138:141], v[130:133], v[82:97]
	s_nop 0
	v_lshl_add_u64 v[54:55], v[142:143], 0, v[174:175]
	v_mul_f32_e32 v56, 0x3c23d70a, v98
	global_store_dwordx4 v[54:55], v[58:61], off nt
	v_max_f32_e32 v56, v98, v56
	v_mul_f32_e32 v57, 0x3c23d70a, v99
	v_max_f32_e32 v57, v99, v57
	v_pk_add_f32 v[34:35], v[34:35], v[56:57]
	v_mul_f32_e32 v56, 0x3c23d70a, v100
	v_max_f32_e32 v56, v100, v56
	v_mul_f32_e32 v57, 0x3c23d70a, v101
	v_max_f32_e32 v58, v101, v101
	v_max_f32_e32 v57, v58, v57
	v_pk_add_f32 v[36:37], v[36:37], v[56:57]
	ds_write_b128 v160, v[34:37] offset:61440
	v_mul_f32_e32 v34, 0x3c23d70a, v102
	v_max_f32_e32 v34, v102, v34
	v_mul_f32_e32 v35, 0x3c23d70a, v103
	v_max_f32_e32 v35, v103, v35
	v_mul_f32_e32 v36, 0x3c23d70a, v104
	v_pk_add_f32 v[34:35], v[38:39], v[34:35]
	v_max_f32_e32 v36, v104, v36
	v_mul_f32_e32 v37, 0x3c23d70a, v105
	v_max_f32_e32 v37, v105, v37
	v_pk_add_f32 v[36:37], v[40:41], v[36:37]
	ds_write_b128 v160, v[34:37] offset:61472
	v_mul_f32_e32 v34, 0x3c23d70a, v106
	v_max_f32_e32 v34, v106, v34
	v_mul_f32_e32 v35, 0x3c23d70a, v107
	v_max_f32_e32 v35, v107, v35
	v_mul_f32_e32 v36, 0x3c23d70a, v108
	v_max_f32_e32 v36, v108, v36
	v_mul_f32_e32 v37, 0x3c23d70a, v109
	v_max_f32_e32 v37, v109, v37
	v_pk_add_f32 v[34:35], v[42:43], v[34:35]
	v_pk_add_f32 v[36:37], v[44:45], v[36:37]
	ds_write_b128 v160, v[34:37] offset:61504
	v_mul_f32_e32 v34, 0x3c23d70a, v110
	v_max_f32_e32 v34, v110, v34
	v_mul_f32_e32 v35, 0x3c23d70a, v111
	v_max_f32_e32 v35, v111, v35
	v_mul_f32_e32 v36, 0x3c23d70a, v112
	v_max_f32_e32 v36, v112, v36
	v_mul_f32_e32 v37, 0x3c23d70a, v113
	v_max_f32_e32 v37, v113, v37
	v_pk_add_f32 v[34:35], v[46:47], v[34:35]
	v_pk_add_f32 v[36:37], v[48:49], v[36:37]
	ds_write_b128 v160, v[34:37] offset:61536
	ds_read_b128 v[34:37], v145 offset:61440
	ds_read_b128 v[38:41], v62 offset:61440
	ds_read_b128 v[42:45], v63 offset:61440
	ds_read_b128 v[46:49], v64 offset:61440
	s_waitcnt lgkmcnt(3)
	global_store_dwordx4 v[0:1], v[34:37], off offset:128 nt
	s_waitcnt lgkmcnt(2)
	global_store_dwordx4 v[50:51], v[38:41], off offset:128 nt
	s_waitcnt lgkmcnt(1)
	global_store_dwordx4 v[52:53], v[42:45], off offset:128 nt
	s_waitcnt lgkmcnt(0)
	global_store_dwordx4 v[54:55], v[46:49], off offset:128 nt
	v_mul_f32_e32 v34, 0x3c23d70a, v82
	v_max_f32_e32 v34, v82, v34
	v_mul_f32_e32 v35, 0x3c23d70a, v83
	v_max_f32_e32 v35, v83, v35
	v_pk_add_f32 v[18:19], v[18:19], v[34:35]
	v_mul_f32_e32 v34, 0x3c23d70a, v84
	v_max_f32_e32 v34, v84, v34
	v_mul_f32_e32 v35, 0x3c23d70a, v85
	v_max_f32_e32 v36, v85, v85
	v_max_f32_e32 v35, v36, v35
	v_pk_add_f32 v[20:21], v[20:21], v[34:35]
	ds_write_b128 v160, v[18:21] offset:61440
	v_mul_f32_e32 v18, 0x3c23d70a, v86
	v_max_f32_e32 v18, v86, v18
	v_mul_f32_e32 v19, 0x3c23d70a, v87
	v_max_f32_e32 v19, v87, v19
	v_mul_f32_e32 v20, 0x3c23d70a, v88
	v_pk_add_f32 v[18:19], v[22:23], v[18:19]
	v_max_f32_e32 v20, v88, v20
	v_mul_f32_e32 v21, 0x3c23d70a, v89
	v_max_f32_e32 v21, v89, v21
	v_pk_add_f32 v[20:21], v[24:25], v[20:21]
	ds_write_b128 v160, v[18:21] offset:61472
	v_mul_f32_e32 v18, 0x3c23d70a, v90
	v_max_f32_e32 v18, v90, v18
	v_mul_f32_e32 v19, 0x3c23d70a, v91
	v_max_f32_e32 v19, v91, v19
	v_mul_f32_e32 v20, 0x3c23d70a, v92
	v_max_f32_e32 v20, v92, v20
	v_mul_f32_e32 v21, 0x3c23d70a, v93
	v_max_f32_e32 v21, v93, v21
	v_pk_add_f32 v[18:19], v[26:27], v[18:19]
	v_pk_add_f32 v[20:21], v[28:29], v[20:21]
	ds_write_b128 v160, v[18:21] offset:61504
	v_mul_f32_e32 v18, 0x3c23d70a, v94
	v_max_f32_e32 v18, v94, v18
	v_mul_f32_e32 v19, 0x3c23d70a, v95
	v_max_f32_e32 v19, v95, v19
	v_mul_f32_e32 v20, 0x3c23d70a, v96
	v_max_f32_e32 v20, v96, v20
	v_mul_f32_e32 v21, 0x3c23d70a, v97
	v_mfma_f32_32x32x16_bf16 v[66:81], v[134:137], v[130:133], v[66:81]
	v_max_f32_e32 v21, v97, v21
	v_add_f32_e64 v18, v30, v18
	v_add_f32_e64 v19, v31, v19
	v_add_f32_e64 v20, v32, v20
	v_add_f32_e64 v21, v33, v21
	ds_write_b128 v160, v[18:21] offset:61536
	ds_read_b128 v[18:21], v145 offset:61440
	ds_read_b128 v[22:25], v62 offset:61440
	ds_read_b128 v[26:29], v63 offset:61440
	ds_read_b128 v[30:33], v64 offset:61440
	s_waitcnt lgkmcnt(3)
	global_store_dwordx4 v[0:1], v[18:21], off offset:256 nt
	s_waitcnt lgkmcnt(2)
	global_store_dwordx4 v[50:51], v[22:25], off offset:256 nt
	s_waitcnt lgkmcnt(1)
	global_store_dwordx4 v[52:53], v[26:29], off offset:256 nt
	s_waitcnt lgkmcnt(0)
	global_store_dwordx4 v[54:55], v[30:33], off offset:256 nt
	v_mul_f32_e32 v18, 0x3c23d70a, v66
	v_max_f32_e32 v18, v66, v18
	v_mul_f32_e32 v19, 0x3c23d70a, v67
	v_max_f32_e32 v19, v67, v19
	v_pk_add_f32 v[2:3], v[2:3], v[18:19]
	v_mul_f32_e32 v18, 0x3c23d70a, v68
	v_max_f32_e32 v18, v68, v18
	v_mul_f32_e32 v19, 0x3c23d70a, v69
	v_max_f32_e32 v20, v69, v69
	v_max_f32_e32 v19, v20, v19
	v_pk_add_f32 v[4:5], v[4:5], v[18:19]
	ds_write_b128 v160, v[2:5] offset:61440
	v_mul_f32_e32 v2, 0x3c23d70a, v70
	v_max_f32_e32 v2, v70, v2
	v_mul_f32_e32 v3, 0x3c23d70a, v71
	v_max_f32_e32 v3, v71, v3
	v_mul_f32_e32 v4, 0x3c23d70a, v72
	v_pk_add_f32 v[2:3], v[6:7], v[2:3]
	v_max_f32_e32 v4, v72, v4
	v_mul_f32_e32 v5, 0x3c23d70a, v73
	v_max_f32_e32 v5, v73, v5
	v_pk_add_f32 v[4:5], v[8:9], v[4:5]
	ds_write_b128 v160, v[2:5] offset:61472
	v_mul_f32_e32 v2, 0x3c23d70a, v74
	v_max_f32_e32 v2, v74, v2
	v_mul_f32_e32 v3, 0x3c23d70a, v75
	v_max_f32_e32 v3, v75, v3
	v_mul_f32_e32 v4, 0x3c23d70a, v76
	v_max_f32_e32 v4, v76, v4
	v_mul_f32_e32 v5, 0x3c23d70a, v77
	v_max_f32_e32 v5, v77, v5
	v_pk_add_f32 v[2:3], v[10:11], v[2:3]
	v_pk_add_f32 v[4:5], v[12:13], v[4:5]
	ds_write_b128 v160, v[2:5] offset:61504
	v_mul_f32_e32 v2, 0x3c23d70a, v78
	v_max_f32_e32 v2, v78, v2
	v_mul_f32_e32 v3, 0x3c23d70a, v79
	v_max_f32_e32 v3, v79, v3
	v_mul_f32_e32 v4, 0x3c23d70a, v80
	v_max_f32_e32 v4, v80, v4
	v_mul_f32_e32 v5, 0x3c23d70a, v81
	v_max_f32_e32 v5, v81, v5
	v_pk_add_f32 v[2:3], v[14:15], v[2:3]
	v_pk_add_f32 v[4:5], v[16:17], v[4:5]
	ds_write_b128 v160, v[2:5] offset:61536
	ds_read_b128 v[2:5], v145 offset:61440
	ds_read_b128 v[6:9], v62 offset:61440
	ds_read_b128 v[10:13], v63 offset:61440
	ds_read_b128 v[14:17], v64 offset:61440
	s_waitcnt lgkmcnt(3)
	global_store_dwordx4 v[0:1], v[2:5], off offset:384 nt
	s_waitcnt lgkmcnt(2)
	global_store_dwordx4 v[50:51], v[6:9], off offset:384 nt
	s_waitcnt lgkmcnt(1)
	global_store_dwordx4 v[52:53], v[10:13], off offset:384 nt
	s_waitcnt lgkmcnt(0)
	global_store_dwordx4 v[54:55], v[14:17], off offset:384 nt
	s_endpgm

_Z16node_post_kernelPKfS0_PKtS0_S2_S0_S0_S0_S0_S0_Pf:
	s_load_dwordx8 s[12:19], s[0:1], 0x10
	s_load_dwordx8 s[20:27], s[0:1], 0x30
	s_lshr_b32 s28, s2, 3
	v_lshlrev_b32_e32 v162, 4, v0
	v_and_b32_e32 v163, 0xff0, v162
	v_add_u32_e32 v163, 0x2000, v163
	v_and_b32_e32 v168, 0xff, v0
	v_lshlrev_b32_e32 v168, 2, v168
	v_lshlrev_b32_e32 v169, 2, v0
	s_mul_i32 s29, s28, 0x3000
	s_lshr_b32 s32, s2, 7
	s_lshl_b32 s32, s32, 17
	s_and_b32 s33, s28, 15
	s_lshl_b32 s33, s33, 13
	s_add_u32 s32, s32, s33
	s_lshl_b32 s33, s2, 11
	s_waitcnt lgkmcnt(0)
	s_add_u32 s30, s16, s29
	s_addc_u32 s31, s17, 0
	s_add_u32 s34, s12, s32
	s_addc_u32 s35, s13, 0
	s_add_u32 s36, s14, s33
	s_addc_u32 s37, s15, 0
	global_load_dwordx4 v[164:167], v162, s[34:35]
	global_load_dwordx4 v[164:167], v162, s[30:31]
	global_load_dwordx4 v[164:167], v163, s[30:31]
	global_load_dword v164, v169, s[36:37]
	global_load_dword v164, v168, s[18:19]
	global_load_dword v164, v168, s[20:21]
	global_load_dword v164, v168, s[22:23]
	global_load_dword v164, v168, s[24:25]
	global_load_dword v164, v168, s[26:27]
	s_load_dwordx4 s[4:7], s[0:1], 0x0
	s_load_dwordx2 s[10:11], s[0:1], 0x10
	s_lshl_b32 s8, s2, 1
	s_bfe_i32 s2, s2, 0x180007
	v_bfe_u32 v19, v0, 6, 1
	s_ashr_i32 s3, s2, 31
	v_or_b32_e32 v2, s8, v19
	s_lshl_b64 s[2:3], s[2:3], 17
	v_ashrrev_i32_e32 v3, 31, v2
	s_waitcnt lgkmcnt(0)
	s_add_u32 s2, s10, s2
	v_lshlrev_b64 v[2:3], 13, v[2:3]
	v_and_b32_e32 v144, 63, v0
	s_addc_u32 s3, s11, s3
	v_lshl_add_u64 v[2:3], s[4:5], 0, v[2:3]
	s_and_b32 s4, s8, 0xffffff00
	v_lshrrev_b32_e32 v1, 6, v0
	v_or_b32_e32 v8, s4, v144
	v_mov_b32_e32 v18, 0
	v_and_b32_e32 v134, 6, v1
	v_ashrrev_i32_e32 v9, 31, v8
	s_ashr_i32 s4, s4, 31
	v_lshlrev_b32_e32 v4, 2, v134
	v_mov_b32_e32 v5, v18
	v_lshl_add_u64 v[10:11], v[8:9], 2, s[6:7]
	v_mov_b32_e32 v9, s4
	v_lshl_add_u64 v[2:3], v[2:3], 0, v[4:5]
	v_lshlrev_b32_e32 v4, 5, v144
	v_lshl_add_u64 v[8:9], v[8:9], 2, s[6:7]
	global_load_dword v38, v[10:11], off
	global_load_dword v39, v[8:9], off offset:256
	v_or_b32_e32 v10, 0x800, v4
	v_mov_b32_e32 v11, v18
	v_lshl_add_u64 v[10:11], v[2:3], 0, v[10:11]
	v_lshl_add_u64 v[6:7], v[2:3], 0, v[4:5]
	global_load_dwordx2 v[20:21], v[10:11], off
	v_or_b32_e32 v10, 0x1000, v4
	v_mov_b32_e32 v11, v18
	global_load_dwordx2 v[6:7], v[6:7], off
	v_lshl_add_u64 v[10:11], v[2:3], 0, v[10:11]
	global_load_dwordx2 v[22:23], v[10:11], off
	global_load_dword v40, v[8:9], off offset:512
	v_or_b32_e32 v4, 0x1800, v4
	v_lshl_add_u64 v[2:3], v[2:3], 0, v[4:5]
	global_load_dword v41, v[8:9], off offset:768
	global_load_dwordx2 v[4:5], v[2:3], off
	v_lshl_or_b32 v24, v1, 10, v144
	v_lshlrev_b32_e32 v142, 4, v24
	v_mov_b32_e32 v143, v18
	v_lshl_add_u64 v[2:3], s[2:3], 0, v[142:143]
	s_movk_i32 s6, 0x1000
	s_load_dwordx2 s[4:5], s[0:1], 0x20
	v_add_co_u32_e32 v8, vcc, s6, v2
	s_movk_i32 s7, 0x2000
	s_nop 0
	v_addc_co_u32_e32 v9, vcc, 0, v3, vcc
	global_load_dwordx4 v[34:37], v[8:9], off
	global_load_dwordx4 v[26:29], v[8:9], off offset:1024
	global_load_dwordx4 v[14:17], v[8:9], off offset:2048
	global_load_dwordx4 v[10:13], v[8:9], off offset:3072
	v_or_b32_e32 v8, 0x200, v24
	v_add_co_u32_e32 v24, vcc, s7, v2
	s_movk_i32 s9, 0x3000
	s_nop 0
	v_addc_co_u32_e32 v25, vcc, 0, v3, vcc
	v_add_co_u32_e32 v30, vcc, s9, v2
	v_lshlrev_b32_e32 v145, 4, v8
	s_nop 0
	v_addc_co_u32_e32 v31, vcc, 0, v3, vcc
	s_waitcnt lgkmcnt(0)
	v_lshl_add_u64 v[2:3], s[4:5], 0, v[142:143]
	v_add_co_u32_e32 v32, vcc, s6, v2
	s_mov_b32 s6, 0xff7fffff
	s_nop 0
	v_addc_co_u32_e32 v33, vcc, 0, v3, vcc
	v_add_co_u32_e32 v46, vcc, s7, v2
	v_lshlrev_b32_e32 v19, 12, v19
	s_nop 0
	v_addc_co_u32_e32 v47, vcc, 0, v3, vcc
	v_add_co_u32_e32 v78, vcc, s9, v2
	v_mov_b32_e32 v2, 0xff7fffff
	s_nop 0
	v_addc_co_u32_e32 v79, vcc, 0, v3, vcc
	v_lshlrev_b32_e32 v134, 9, v134
	v_and_b32_e32 v152, 15, v0
	s_waitcnt vmcnt(11)
	v_cmp_neq_f32_e32 vcc, 0, v38
	s_waitcnt vmcnt(8)
	s_nop 0
	v_cndmask_b32_e32 v3, v2, v6, vcc
	v_cndmask_b32_e32 v6, v2, v7, vcc
	v_cmp_neq_f32_e32 vcc, 0, v39
	s_nop 1
	v_cndmask_b32_e32 v7, v2, v20, vcc
	v_cndmask_b32_e32 v8, v2, v21, vcc
	s_waitcnt vmcnt(6)
	v_cmp_neq_f32_e32 vcc, 0, v40
	v_max3_f32 v9, v3, s6, v7
	v_max3_f32 v20, v6, s6, v8
	v_cndmask_b32_e32 v21, v2, v22, vcc
	v_cndmask_b32_e32 v22, v2, v23, vcc
	s_waitcnt vmcnt(5)
	v_cmp_neq_f32_e32 vcc, 0, v41
	s_waitcnt vmcnt(4)
	s_nop 0
	v_cndmask_b32_e32 v4, v2, v4, vcc
	v_cndmask_b32_e32 v2, v2, v5, vcc
	v_max3_f32 v5, v9, v21, v4
	v_max3_f32 v9, v20, v22, v2
	s_nop 0
	v_mov_b32_dpp v20, v5 quad_perm:[1,0,3,2] row_mask:0xf bank_mask:0xf bound_ctrl:1
	v_max_f32_e32 v20, v20, v20
	v_max_f32_e32 v5, v5, v20
	s_nop 1
	v_mov_b32_dpp v20, v5 quad_perm:[2,3,0,1] row_mask:0xf bank_mask:0xf bound_ctrl:1
	v_max_f32_e32 v20, v20, v20
	v_max_f32_e32 v5, v5, v20
	s_nop 1
	v_mov_b32_dpp v20, v5 row_half_mirror row_mask:0xf bank_mask:0xf bound_ctrl:1
	v_max_f32_e32 v20, v20, v20
	v_max_f32_e32 v5, v5, v20
	s_nop 1
	v_mov_b32_dpp v20, v5 row_mirror row_mask:0xf bank_mask:0xf bound_ctrl:1
	v_max_f32_e32 v20, v20, v20
	v_max_f32_e32 v5, v5, v20
	v_mov_b32_e32 v20, v5
	s_nop 1
	v_permlane16_swap_b32_e32 v5, v20
	v_max_f32_e32 v20, v20, v20
	v_max_f32_e32 v5, v5, v5
	v_max_f32_e32 v5, v5, v20
	v_mov_b32_e32 v20, v5
	s_nop 1
	v_permlane32_swap_b32_e32 v5, v20
	v_max_f32_e32 v20, v20, v20
	v_max_f32_e32 v5, v5, v5
	v_max_f32_e32 v5, v5, v20
	v_mov_b32_dpp v20, v9 quad_perm:[1,0,3,2] row_mask:0xf bank_mask:0xf bound_ctrl:1
	v_max_f32_e32 v20, v20, v20
	v_max_f32_e32 v9, v9, v20
	v_sub_f32_e32 v3, v3, v5
	v_mul_f32_e32 v3, 0x3fb8aa3b, v3
	v_mov_b32_dpp v20, v9 quad_perm:[2,3,0,1] row_mask:0xf bank_mask:0xf bound_ctrl:1
	v_max_f32_e32 v20, v20, v20
	v_max_f32_e32 v9, v9, v20
	v_sub_f32_e32 v4, v4, v5
	v_mul_f32_e32 v4, 0x3fb8aa3b, v4
	v_mov_b32_dpp v20, v9 row_half_mirror row_mask:0xf bank_mask:0xf bound_ctrl:1
	v_max_f32_e32 v20, v20, v20
	v_max_f32_e32 v9, v9, v20
	v_exp_f32_e32 v139, v4
	s_nop 0
	v_mov_b32_dpp v20, v9 row_mirror row_mask:0xf bank_mask:0xf bound_ctrl:1
	v_max_f32_e32 v20, v20, v20
	v_max_f32_e32 v9, v9, v20
	v_mov_b32_e32 v20, v9
	s_nop 1
	v_permlane16_swap_b32_e32 v9, v20
	v_max_f32_e32 v20, v20, v20
	v_max_f32_e32 v9, v9, v9
	v_max_f32_e32 v9, v9, v20
	v_mov_b32_e32 v20, v9
	s_nop 1
	v_permlane32_swap_b32_e32 v9, v20
	v_max_f32_e32 v20, v20, v20
	v_max_f32_e32 v9, v9, v9
	v_max_f32_e32 v9, v9, v20
	v_exp_f32_e32 v20, v3
	v_sub_f32_e32 v3, v6, v9
	v_mul_f32_e32 v3, 0x3fb8aa3b, v3
	v_exp_f32_e32 v135, v3
	v_sub_f32_e32 v3, v7, v5
	v_mul_f32_e32 v3, 0x3fb8aa3b, v3
	v_sub_f32_e32 v7, v21, v5
	v_exp_f32_e32 v136, v3
	v_mul_f32_e32 v7, 0x3fb8aa3b, v7
	v_sub_f32_e32 v3, v8, v9
	v_exp_f32_e32 v21, v7
	v_mul_f32_e32 v3, 0x3fb8aa3b, v3
	v_exp_f32_e32 v137, v3
	v_add_f32_e32 v3, 0, v20
	v_sub_f32_e32 v2, v2, v9
	v_add_f32_e32 v3, v3, v136
	v_mul_f32_e32 v2, 0x3fb8aa3b, v2
	v_exp_f32_e32 v140, v2
	v_add_f32_e32 v2, v3, v21
	v_add_f32_e32 v2, v2, v139
	v_sub_f32_e32 v7, v22, v9
	v_mul_f32_e32 v7, 0x3fb8aa3b, v7
	v_add_f32_dpp v2, v2, v2 quad_perm:[1,0,3,2] row_mask:0xf bank_mask:0xf bound_ctrl:1
	v_exp_f32_e32 v138, v7
	v_add_f32_e32 v6, 0, v135
	v_add_f32_dpp v2, v2, v2 quad_perm:[2,3,0,1] row_mask:0xf bank_mask:0xf bound_ctrl:1
	v_add_f32_e32 v6, v6, v137
	v_add_f32_e32 v3, v6, v138
	v_add_f32_dpp v2, v2, v2 row_half_mirror row_mask:0xf bank_mask:0xf bound_ctrl:1
	v_add_f32_e32 v3, v3, v140
	s_nop 0
	v_add_f32_dpp v2, v2, v2 row_mirror row_mask:0xf bank_mask:0xf bound_ctrl:1
	v_mov_b32_e32 v4, v2
	s_nop 1
	v_permlane16_swap_b32_e32 v2, v4
	v_add_f32_e32 v2, v2, v4
	v_mov_b32_e32 v4, v2
	s_nop 1
	v_permlane32_swap_b32_e32 v2, v4
	v_add_f32_e32 v141, v2, v4
	s_nop 0
	v_add_f32_dpp v2, v3, v3 quad_perm:[1,0,3,2] row_mask:0xf bank_mask:0xf bound_ctrl:1
	v_div_scale_f32 v143, s[6:7], v141, v141, 1.0
	s_nop 0
	v_add_f32_dpp v2, v2, v2 quad_perm:[2,3,0,1] row_mask:0xf bank_mask:0xf bound_ctrl:1
	v_rcp_f32_e32 v146, v143
	v_div_scale_f32 v148, vcc, 1.0, v141, 1.0
	v_add_f32_dpp v2, v2, v2 row_half_mirror row_mask:0xf bank_mask:0xf bound_ctrl:1
	s_nop 1
	v_add_f32_dpp v2, v2, v2 row_mirror row_mask:0xf bank_mask:0xf bound_ctrl:1
	v_mov_b32_e32 v3, v2
	s_nop 1
	v_permlane16_swap_b32_e32 v2, v3
	v_add_f32_e32 v2, v2, v3
	v_mov_b32_e32 v3, v2
	s_nop 1
	v_permlane32_swap_b32_e32 v2, v3
	v_add_f32_e32 v147, v2, v3
	v_fma_f32 v2, -v143, v146, 1.0
	v_fmac_f32_e32 v146, v2, v146
	global_load_dwordx4 v[90:93], v[24:25], off offset:1024
	global_load_dwordx4 v[82:85], v[24:25], off offset:2048
	global_load_dwordx4 v[74:77], v[24:25], off offset:3072
	global_load_dwordx4 v[66:69], v[30:31], off
	global_load_dwordx4 v[58:61], v[30:31], off offset:1024
	global_load_dwordx4 v[50:53], v[30:31], off offset:2048
	global_load_dwordx4 v[42:45], v[30:31], off offset:3072
	global_load_dwordx4 v[54:57], v[32:33], off
	global_load_dwordx4 v[38:41], v[32:33], off offset:1024
	global_load_dwordx4 v[6:9], v[32:33], off offset:2048
	global_load_dwordx4 v[2:5], v[32:33], off offset:3072
	global_load_dwordx4 v[102:105], v[46:47], off offset:1024
	global_load_dwordx4 v[86:89], v[46:47], off offset:2048
	global_load_dwordx4 v[70:73], v[46:47], off offset:3072
	global_load_dwordx4 v[62:65], v[78:79], off
	s_nop 0
	global_load_dwordx4 v[46:49], v[78:79], off offset:1024
	global_load_dwordx4 v[30:33], v[78:79], off offset:2048
	global_load_dwordx4 v[22:25], v[78:79], off offset:3072
	global_load_dwordx4 v[122:125], v142, s[2:3]
	global_load_dwordx4 v[114:117], v142, s[2:3] offset:1024
	global_load_dwordx4 v[106:109], v142, s[2:3] offset:2048
	global_load_dwordx4 v[98:101], v142, s[2:3] offset:3072
	global_load_dwordx4 v[126:129], v142, s[4:5]
	global_load_dwordx4 v[110:113], v142, s[4:5] offset:1024
	global_load_dwordx4 v[94:97], v142, s[4:5] offset:2048
	global_load_dwordx4 v[78:81], v142, s[4:5] offset:3072
	global_load_dwordx4 v[130:133], v145, s[2:3]
	global_load_dwordx4 v[118:121], v145, s[4:5]
	v_mul_f32_e32 v149, v148, v146
	v_fma_f32 v150, -v143, v149, v148
	v_fmac_f32_e32 v149, v150, v146
	v_fma_f32 v143, -v143, v149, v148
	v_div_scale_f32 v148, s[2:3], v147, v147, 1.0
	v_rcp_f32_e32 v150, v148
	v_div_fmas_f32 v143, v143, v146, v149
	v_div_fixup_f32 v141, v143, v141, 1.0
	v_mul_f32_e32 v20, v141, v20
	v_fma_f32 v143, -v148, v150, 1.0
	v_fmac_f32_e32 v150, v143, v150
	v_div_scale_f32 v143, vcc, 1.0, v147, 1.0
	v_mul_f32_e32 v146, v143, v150
	v_fma_f32 v149, -v148, v146, v143
	v_fmac_f32_e32 v146, v149, v150
	v_fma_f32 v143, -v148, v146, v143
	v_div_fmas_f32 v143, v143, v150, v146
	v_div_fixup_f32 v143, v143, v147, 1.0
	v_lshlrev_b32_e32 v146, 1, v144
	v_lshlrev_b32_e32 v147, 9, v1
	v_bfe_u32 v148, v20, 16, 1
	s_movk_i32 s2, 0x7fff
	v_add3_u32 v20, v20, v148, s2
	v_or3_b32 v148, v147, v19, v146
	v_or3_b32 v19, v19, v134, v146
	ds_write_b16_d16_hi v19, v20
	v_mul_f32_e32 v20, v143, v135
	v_bfe_u32 v134, v20, 16, 1
	v_add3_u32 v20, v20, v134, s2
	v_or_b32_e32 v134, 0x200, v148
	ds_write_b16_d16_hi v134, v20
	v_mul_f32_e32 v20, v141, v136
	v_bfe_u32 v134, v20, 16, 1
	v_add3_u32 v20, v20, v134, s2
	ds_write_b16_d16_hi v19, v20 offset:128
	v_mul_f32_e32 v20, v143, v137
	v_bfe_u32 v134, v20, 16, 1
	v_add3_u32 v20, v20, v134, s2
	v_or_b32_e32 v134, 0x280, v148
	ds_write_b16_d16_hi v134, v20
	v_mul_f32_e32 v20, v141, v21
	v_bfe_u32 v21, v20, 16, 1
	v_add3_u32 v20, v20, v21, s2
	ds_write_b16_d16_hi v19, v20 offset:256
	v_mul_f32_e32 v20, v143, v138
	v_bfe_u32 v21, v20, 16, 1
	v_add3_u32 v20, v20, v21, s2
	v_or_b32_e32 v21, 0x300, v148
	ds_write_b16_d16_hi v21, v20
	v_mul_f32_e32 v20, v141, v139
	v_bfe_u32 v21, v20, 16, 1
	v_add3_u32 v20, v20, v21, s2
	ds_write_b16_d16_hi v19, v20 offset:384
	v_mul_f32_e32 v19, v143, v140
	v_bfe_u32 v20, v19, 16, 1
	v_add3_u32 v19, v19, v20, s2
	v_or_b32_e32 v20, 0x380, v148
	ds_write_b16_d16_hi v20, v19
	v_lshrrev_b32_e32 v20, 1, v0
	v_and_b32_e32 v20, 24, v20
	v_lshlrev_b32_e32 v19, 12, v152
	v_lshlrev_b32_e32 v153, 1, v20
	v_or3_b32 v143, v147, v19, v153
	v_cmp_gt_u32_e64 s[2:3], 2, v152
	v_mov_b32_e32 v138, 0
	v_mov_b32_e32 v139, 0
	v_mov_b32_e32 v140, 0
	v_mov_b32_e32 v141, 0
	s_waitcnt lgkmcnt(0)
	s_barrier
	s_and_saveexec_b64 s[6:7], s[2:3]
	ds_read_b128 v[138:141], v143
	s_or_b64 exec, exec, s[6:7]
	s_waitcnt vmcnt(9) lgkmcnt(0)
	v_mfma_f32_16x16x32_bf16 v[134:137], v[122:125], v[138:141], 0
	v_mov_b32_e32 v19, 0
	v_mov_b32_e32 v20, 0
	v_mov_b32_e32 v21, 0
	s_waitcnt vmcnt(1)
	v_mfma_f32_16x16x32_bf16 v[130:133], v[130:133], v[138:141], 0
	s_and_saveexec_b64 s[6:7], s[2:3]
	ds_read_b128 v[18:21], v143 offset:64
	s_or_b64 exec, exec, s[6:7]
	s_waitcnt lgkmcnt(0)
	v_mfma_f32_16x16x32_bf16 v[134:137], v[114:117], v[18:21], v[134:137]
	v_mov_b32_e32 v122, 0
	v_mov_b32_e32 v114, 0
	v_mov_b32_e32 v115, 0
	v_mfma_f32_16x16x32_bf16 v[18:21], v[90:93], v[18:21], v[130:133]
	v_mov_b32_e32 v116, 0
	v_mov_b32_e32 v117, 0
	s_and_saveexec_b64 s[6:7], s[2:3]
	ds_read_b128 v[114:117], v143 offset:128
	s_or_b64 exec, exec, s[6:7]
	s_waitcnt lgkmcnt(0)
	v_mfma_f32_16x16x32_bf16 v[90:93], v[106:109], v[114:117], v[134:137]
	v_mov_b32_e32 v123, 0
	v_mov_b32_e32 v124, 0
	v_mov_b32_e32 v125, 0
	v_mfma_f32_16x16x32_bf16 v[106:109], v[82:85], v[114:117], v[18:21]
	s_and_saveexec_b64 s[6:7], s[2:3]
	ds_read_b128 v[122:125], v143 offset:192
	s_or_b64 exec, exec, s[6:7]
	s_waitcnt lgkmcnt(0)
	v_mfma_f32_16x16x32_bf16 v[98:101], v[98:101], v[122:125], v[90:93]
	v_mov_b32_e32 v18, 0
	v_mov_b32_e32 v82, 0
	v_mov_b32_e32 v83, 0
	v_mfma_f32_16x16x32_bf16 v[90:93], v[74:77], v[122:125], v[106:109]
	v_mov_b32_e32 v84, 0
	v_mov_b32_e32 v85, 0
	s_and_saveexec_b64 s[6:7], s[2:3]
	ds_read_b128 v[82:85], v143 offset:256
	s_or_b64 exec, exec, s[6:7]
	s_waitcnt lgkmcnt(0)
	v_mfma_f32_16x16x32_bf16 v[74:77], v[34:37], v[82:85], v[98:101]
	v_mov_b32_e32 v19, 0
	v_mov_b32_e32 v20, 0
	v_mov_b32_e32 v21, 0
	v_mfma_f32_16x16x32_bf16 v[66:69], v[66:69], v[82:85], v[90:93]
	s_and_saveexec_b64 s[6:7], s[2:3]
	ds_read_b128 v[18:21], v143 offset:320
	s_or_b64 exec, exec, s[6:7]
	s_waitcnt lgkmcnt(0)
	v_mfma_f32_16x16x32_bf16 v[74:77], v[26:29], v[18:21], v[74:77]
	v_mov_b32_e32 v34, 0
	v_mov_b32_e32 v26, 0
	v_mov_b32_e32 v27, 0
	v_mfma_f32_16x16x32_bf16 v[18:21], v[58:61], v[18:21], v[66:69]
	v_mov_b32_e32 v28, 0
	v_mov_b32_e32 v29, 0
	s_and_saveexec_b64 s[6:7], s[2:3]
	ds_read_b128 v[26:29], v143 offset:384
	s_or_b64 exec, exec, s[6:7]
	s_waitcnt lgkmcnt(0)
	v_mfma_f32_16x16x32_bf16 v[14:17], v[14:17], v[26:29], v[74:77]
	v_mov_b32_e32 v35, 0
	v_mov_b32_e32 v36, 0
	v_mov_b32_e32 v37, 0
	v_mfma_f32_16x16x32_bf16 v[18:21], v[50:53], v[26:29], v[18:21]
	s_and_saveexec_b64 s[6:7], s[2:3]
	ds_read_b128 v[34:37], v143 offset:448
	s_or_b64 exec, exec, s[6:7]
	s_waitcnt lgkmcnt(0)
	v_mfma_f32_16x16x32_bf16 v[14:17], v[10:13], v[34:37], v[14:17]
	v_lshrrev_b32_e32 v155, 4, v144
	v_mfma_f32_16x16x32_bf16 v[10:13], v[42:45], v[34:37], v[18:21]
	s_and_saveexec_b64 s[6:7], s[2:3]
	s_cbranch_execz .LBB2_18
	s_nop 0
	v_lshlrev_b32_e32 v18, 9, v152
	v_and_b32_e32 v19, 0x1c0, v0
	v_lshlrev_b32_e32 v20, 3, v155
	v_or3_b32 v18, v18, v19, v20
	v_mov_b32_e32 v19, 1
	v_and_b32_sdwa v20, v16, v19 dst_sel:DWORD dst_unused:UNUSED_PAD src0_sel:WORD_1 src1_sel:DWORD
	s_movk_i32 s9, 0x7fff
	v_and_b32_sdwa v21, v14, v19 dst_sel:DWORD dst_unused:UNUSED_PAD src0_sel:WORD_1 src1_sel:DWORD
	v_add3_u32 v16, v16, v20, s9
	v_and_b32_sdwa v20, v17, v19 dst_sel:DWORD dst_unused:UNUSED_PAD src0_sel:WORD_1 src1_sel:DWORD
	v_add3_u32 v14, v14, v21, s9
	v_and_b32_sdwa v21, v15, v19 dst_sel:DWORD dst_unused:UNUSED_PAD src0_sel:WORD_1 src1_sel:DWORD
	v_add3_u32 v17, v17, v20, s9
	v_add3_u32 v15, v15, v21, s9
	v_and_b32_e32 v17, 0xffff0000, v17
	v_and_b32_e32 v20, 0xffff0000, v15
	v_or_b32_sdwa v15, v17, v16 dst_sel:DWORD dst_unused:UNUSED_PAD src0_sel:DWORD src1_sel:WORD_1
	v_and_b32_sdwa v16, v12, v19 dst_sel:DWORD dst_unused:UNUSED_PAD src0_sel:WORD_1 src1_sel:DWORD
	v_and_b32_sdwa v17, v10, v19 dst_sel:DWORD dst_unused:UNUSED_PAD src0_sel:WORD_1 src1_sel:DWORD
	v_add3_u32 v10, v10, v17, s9
	v_add3_u32 v12, v12, v16, s9
	v_and_b32_sdwa v16, v13, v19 dst_sel:DWORD dst_unused:UNUSED_PAD src0_sel:WORD_1 src1_sel:DWORD
	v_and_b32_sdwa v17, v11, v19 dst_sel:DWORD dst_unused:UNUSED_PAD src0_sel:WORD_1 src1_sel:DWORD
	v_add3_u32 v13, v13, v16, s9
	v_add3_u32 v11, v11, v17, s9
	v_and_b32_e32 v13, 0xffff0000, v13
	v_and_b32_e32 v16, 0xffff0000, v11
	v_or_b32_sdwa v14, v20, v14 dst_sel:DWORD dst_unused:UNUSED_PAD src0_sel:DWORD src1_sel:WORD_1
	v_or_b32_sdwa v11, v13, v12 dst_sel:DWORD dst_unused:UNUSED_PAD src0_sel:DWORD src1_sel:WORD_1
	v_or_b32_sdwa v10, v16, v10 dst_sel:DWORD dst_unused:UNUSED_PAD src0_sel:DWORD src1_sel:WORD_1
	v_add_u32_e32 v12, 0x2800, v18
	ds_write2_b64 v12, v[14:15], v[10:11] offset1:4
